# GEMM loops: a priority flip (s_setprio 0 / 1) after every 8 MFMAs of a phase instead of every 16
# speedup vs baseline: 1.0041x; 1.0041x over previous
.LBB0_477:
	s_add_u32 s2, s34, 0x80
	s_addc_u32 s3, s35, 0
	s_cmp_eq_u32 s45, 28
	s_cselect_b32 s39, s6, s3
	s_cselect_b32 s38, s7, s2
	s_cselect_b32 s37, s40, s43
	s_cselect_b32 s36, s41, s42
	s_add_i32 s2, 0, 0x10000
	v_add_u32_e32 v2, s2, v180
	s_add_i32 s46, 0, 0x14000
	ds_read_b128 v[148:151], v2
	s_waitcnt lgkmcnt(0)
	ds_read_b128 v[152:155], v2 offset:1024
	ds_read_b128 v[156:159], v2 offset:2048
	ds_read_b128 v[160:163], v2 offset:3072
	v_add_u32_e32 v2, s46, v180
	ds_read_b128 v[164:167], v2
	ds_read_b128 v[168:171], v2 offset:1024
	ds_read_b128 v[172:175], v2 offset:2048
	ds_read_b128 v[182:185], v2 offset:3072
	v_lshl_add_u64 v[176:177], s[34:35], 0, v[146:147]
	s_add_i32 m0, s16, 0xc000
	ds_read_b128 v[190:193], v181
	ds_read_b128 v[212:215], v181 offset:1024
	ds_read_b128 v[216:219], v181 offset:2048
	ds_read_b128 v[224:227], v181 offset:3072
	ds_read_b128 v[228:231], v181 offset:4096
	ds_read_b128 v[232:235], v181 offset:5120
	ds_read_b128 v[236:239], v181 offset:6144
	ds_read_b128 v[240:243], v181 offset:7168
	global_load_lds_dwordx4 v[176:177], off
	v_lshl_add_u64 v[176:177], s[34:35], 0, v[144:145]
	s_add_i32 m0, s16, 0xe000
	s_nop 0
	global_load_lds_dwordx4 v[176:177], off
	s_waitcnt vmcnt(8)
	s_waitcnt lgkmcnt(0)
	s_barrier
	s_setprio 1
	s_waitcnt lgkmcnt(0)
	v_mfma_f32_16x16x32_bf16 v[128:131], v[148:151], v[190:193], v[128:131]
	v_mfma_f32_16x16x32_bf16 v[124:127], v[156:159], v[190:193], v[124:127]
	v_mfma_f32_16x16x32_bf16 v[112:115], v[148:151], v[216:219], v[112:115]
	v_mfma_f32_16x16x32_bf16 v[108:111], v[156:159], v[216:219], v[108:111]
	v_mfma_f32_16x16x32_bf16 v[96:99], v[148:151], v[228:231], v[96:99]
	v_mfma_f32_16x16x32_bf16 v[92:95], v[156:159], v[228:231], v[92:95]
	v_mfma_f32_16x16x32_bf16 v[80:83], v[148:151], v[236:239], v[80:83]
	v_mfma_f32_16x16x32_bf16 v[76:79], v[156:159], v[236:239], v[76:79]
	s_setprio 0
	s_setprio 1
	v_mfma_f32_16x16x32_bf16 v[128:131], v[152:155], v[212:215], v[128:131]
	v_mfma_f32_16x16x32_bf16 v[124:127], v[160:163], v[212:215], v[124:127]
	v_mfma_f32_16x16x32_bf16 v[112:115], v[152:155], v[224:227], v[112:115]
	v_mfma_f32_16x16x32_bf16 v[108:111], v[160:163], v[224:227], v[108:111]
	v_mfma_f32_16x16x32_bf16 v[96:99], v[152:155], v[232:235], v[96:99]
	v_mfma_f32_16x16x32_bf16 v[92:95], v[160:163], v[232:235], v[92:95]
	v_mfma_f32_16x16x32_bf16 v[80:83], v[152:155], v[240:243], v[80:83]
	v_mfma_f32_16x16x32_bf16 v[76:79], v[160:163], v[240:243], v[76:79]
	s_setprio 0
	s_setprio 1
	v_mfma_f32_16x16x32_bf16 v[120:123], v[164:167], v[190:193], v[120:123]
	v_mfma_f32_16x16x32_bf16 v[116:119], v[172:175], v[190:193], v[116:119]
	v_mfma_f32_16x16x32_bf16 v[104:107], v[164:167], v[216:219], v[104:107]
	v_mfma_f32_16x16x32_bf16 v[100:103], v[172:175], v[216:219], v[100:103]
	v_mfma_f32_16x16x32_bf16 v[88:91], v[164:167], v[228:231], v[88:91]
	v_mfma_f32_16x16x32_bf16 v[84:87], v[172:175], v[228:231], v[84:87]
	v_mfma_f32_16x16x32_bf16 v[72:75], v[164:167], v[236:239], v[72:75]
	v_mfma_f32_16x16x32_bf16 v[68:71], v[172:175], v[236:239], v[68:71]
	s_setprio 0
	s_setprio 1
	v_mfma_f32_16x16x32_bf16 v[120:123], v[168:171], v[212:215], v[120:123]
	v_mfma_f32_16x16x32_bf16 v[116:119], v[182:185], v[212:215], v[116:119]
	v_mfma_f32_16x16x32_bf16 v[104:107], v[168:171], v[224:227], v[104:107]
	v_mfma_f32_16x16x32_bf16 v[100:103], v[182:185], v[224:227], v[100:103]
	v_mfma_f32_16x16x32_bf16 v[88:91], v[168:171], v[232:235], v[88:91]
	v_mfma_f32_16x16x32_bf16 v[84:87], v[182:185], v[232:235], v[84:87]
	v_mfma_f32_16x16x32_bf16 v[72:75], v[168:171], v[240:243], v[72:75]
	v_mfma_f32_16x16x32_bf16 v[68:71], v[182:185], v[240:243], v[68:71]
	s_setprio 0
	s_barrier
	s_add_i32 s2, s2, s15
	v_lshl_add_u64 v[176:177], s[36:37], 0, v[132:133]
	s_mov_b32 m0, s2
	ds_read_b128 v[190:193], v181 offset:16384
	ds_read_b128 v[212:215], v181 offset:17408
	ds_read_b128 v[216:219], v181 offset:18432
	ds_read_b128 v[224:227], v181 offset:19456
	ds_read_b128 v[228:231], v181 offset:20480
	ds_read_b128 v[232:235], v181 offset:21504
	ds_read_b128 v[236:239], v181 offset:22528
	ds_read_b128 v[240:243], v181 offset:23552
	global_load_lds_dwordx4 v[176:177], off
	s_add_i32 m0, s2, 0x2000
	s_add_u32 s2, s36, 0x80000
	v_lshl_add_u64 v[186:187], s[36:37], 0, v[134:135]
	s_addc_u32 s3, s37, 0
	s_add_i32 s46, s46, s15
	global_load_lds_dwordx4 v[186:187], off
	v_lshl_add_u64 v[194:195], s[2:3], 0, v[132:133]
	s_mov_b32 m0, s46
	v_lshl_add_u64 v[244:245], s[38:39], 0, v[138:139]
	global_load_lds_dwordx4 v[194:195], off
	v_lshl_add_u64 v[194:195], s[2:3], 0, v[134:135]
	s_add_i32 m0, s46, 0x2000
	s_nop 0
	global_load_lds_dwordx4 v[194:195], off
	v_lshl_add_u64 v[194:195], s[38:39], 0, v[136:137]
	s_mov_b32 m0, s16
	s_nop 0
	global_load_lds_dwordx4 v[194:195], off
	s_mov_b32 m0, s17
	s_nop 0
	global_load_lds_dwordx4 v[244:245], off
	s_waitcnt vmcnt(8)
	s_waitcnt lgkmcnt(0)
	s_barrier
	s_setprio 1
	s_waitcnt lgkmcnt(0)
	v_mfma_f32_16x16x32_bf16 v[64:67], v[148:151], v[190:193], v[64:67]
	v_mfma_f32_16x16x32_bf16 v[60:63], v[156:159], v[190:193], v[60:63]
	v_mfma_f32_16x16x32_bf16 v[48:51], v[148:151], v[216:219], v[48:51]
	v_mfma_f32_16x16x32_bf16 v[44:47], v[156:159], v[216:219], v[44:47]
	v_mfma_f32_16x16x32_bf16 v[32:35], v[148:151], v[228:231], v[32:35]
	v_mfma_f32_16x16x32_bf16 v[28:31], v[156:159], v[228:231], v[28:31]
	v_mfma_f32_16x16x32_bf16 v[16:19], v[148:151], v[236:239], v[16:19]
	v_mfma_f32_16x16x32_bf16 v[4:7], v[156:159], v[236:239], v[4:7]
	s_setprio 0
	s_setprio 1
	v_mfma_f32_16x16x32_bf16 v[64:67], v[152:155], v[212:215], v[64:67]
	v_mfma_f32_16x16x32_bf16 v[60:63], v[160:163], v[212:215], v[60:63]
	v_mfma_f32_16x16x32_bf16 v[48:51], v[152:155], v[224:227], v[48:51]
	v_mfma_f32_16x16x32_bf16 v[44:47], v[160:163], v[224:227], v[44:47]
	v_mfma_f32_16x16x32_bf16 v[32:35], v[152:155], v[232:235], v[32:35]
	v_mfma_f32_16x16x32_bf16 v[28:31], v[160:163], v[232:235], v[28:31]
	v_mfma_f32_16x16x32_bf16 v[16:19], v[152:155], v[240:243], v[16:19]
	v_mfma_f32_16x16x32_bf16 v[4:7], v[160:163], v[240:243], v[4:7]
	s_setprio 0
	s_setprio 1
	v_mfma_f32_16x16x32_bf16 v[52:55], v[164:167], v[190:193], v[52:55]
	v_mfma_f32_16x16x32_bf16 v[56:59], v[172:175], v[190:193], v[56:59]
	v_mfma_f32_16x16x32_bf16 v[36:39], v[164:167], v[216:219], v[36:39]
	v_mfma_f32_16x16x32_bf16 v[40:43], v[172:175], v[216:219], v[40:43]
	v_mfma_f32_16x16x32_bf16 v[20:23], v[164:167], v[228:231], v[20:23]
	v_mfma_f32_16x16x32_bf16 v[24:27], v[172:175], v[228:231], v[24:27]
	v_mfma_f32_16x16x32_bf16 v[8:11], v[164:167], v[236:239], v[8:11]
	v_mfma_f32_16x16x32_bf16 v[12:15], v[172:175], v[236:239], v[12:15]
	s_setprio 0
	s_setprio 1
	v_mfma_f32_16x16x32_bf16 v[52:55], v[168:171], v[212:215], v[52:55]
	v_mfma_f32_16x16x32_bf16 v[56:59], v[182:185], v[212:215], v[56:59]
	v_mfma_f32_16x16x32_bf16 v[36:39], v[168:171], v[224:227], v[36:39]
	v_mfma_f32_16x16x32_bf16 v[40:43], v[182:185], v[224:227], v[40:43]
	v_mfma_f32_16x16x32_bf16 v[20:23], v[168:171], v[232:235], v[20:23]
	v_mfma_f32_16x16x32_bf16 v[24:27], v[182:185], v[232:235], v[24:27]
	v_mfma_f32_16x16x32_bf16 v[8:11], v[168:171], v[240:243], v[8:11]
	v_mfma_f32_16x16x32_bf16 v[12:15], v[182:185], v[240:243], v[12:15]
	s_setprio 0
	s_barrier
	s_add_i32 s2, 0, 0x18000
	v_add_u32_e32 v2, s2, v180
	s_add_i32 s46, 0, 0x1c000
	ds_read_b128 v[148:151], v2
	ds_read_b128 v[152:155], v2 offset:1024
	ds_read_b128 v[156:159], v2 offset:2048
	ds_read_b128 v[160:163], v2 offset:3072
	v_add_u32_e32 v2, s46, v180
	ds_read_b128 v[164:167], v2
	ds_read_b128 v[168:171], v2 offset:1024
	ds_read_b128 v[172:175], v2 offset:2048
	ds_read_b128 v[182:185], v2 offset:3072
	s_mov_b32 m0, s18
	v_lshl_add_u64 v[246:247], s[38:39], 0, v[140:141]
	ds_read_b128 v[190:193], v181 offset:32768
	ds_read_b128 v[212:215], v181 offset:33792
	ds_read_b128 v[216:219], v181 offset:34816
	ds_read_b128 v[224:227], v181 offset:35840
	ds_read_b128 v[228:231], v181 offset:36864
	ds_read_b128 v[232:235], v181 offset:37888
	ds_read_b128 v[236:239], v181 offset:38912
	ds_read_b128 v[240:243], v181 offset:39936
	global_load_lds_dwordx4 v[246:247], off
	v_lshl_add_u64 v[246:247], s[38:39], 0, v[142:143]
	s_mov_b32 m0, s19
	s_nop 0
	global_load_lds_dwordx4 v[246:247], off
	s_waitcnt vmcnt(8)
	s_waitcnt lgkmcnt(0)
	s_barrier
	s_setprio 1
	s_waitcnt lgkmcnt(0)
	v_mfma_f32_16x16x32_bf16 v[128:131], v[148:151], v[190:193], v[128:131]
	v_mfma_f32_16x16x32_bf16 v[124:127], v[156:159], v[190:193], v[124:127]
	v_mfma_f32_16x16x32_bf16 v[112:115], v[148:151], v[216:219], v[112:115]
	v_mfma_f32_16x16x32_bf16 v[108:111], v[156:159], v[216:219], v[108:111]
	v_mfma_f32_16x16x32_bf16 v[96:99], v[148:151], v[228:231], v[96:99]
	v_mfma_f32_16x16x32_bf16 v[92:95], v[156:159], v[228:231], v[92:95]
	v_mfma_f32_16x16x32_bf16 v[80:83], v[148:151], v[236:239], v[80:83]
	v_mfma_f32_16x16x32_bf16 v[76:79], v[156:159], v[236:239], v[76:79]
	s_setprio 0
	s_setprio 1
	v_mfma_f32_16x16x32_bf16 v[128:131], v[152:155], v[212:215], v[128:131]
	v_mfma_f32_16x16x32_bf16 v[124:127], v[160:163], v[212:215], v[124:127]
	v_mfma_f32_16x16x32_bf16 v[112:115], v[152:155], v[224:227], v[112:115]
	v_mfma_f32_16x16x32_bf16 v[108:111], v[160:163], v[224:227], v[108:111]
	v_mfma_f32_16x16x32_bf16 v[96:99], v[152:155], v[232:235], v[96:99]
	v_mfma_f32_16x16x32_bf16 v[92:95], v[160:163], v[232:235], v[92:95]
	v_mfma_f32_16x16x32_bf16 v[80:83], v[152:155], v[240:243], v[80:83]
	v_mfma_f32_16x16x32_bf16 v[76:79], v[160:163], v[240:243], v[76:79]
	s_setprio 0
	s_setprio 1
	v_mfma_f32_16x16x32_bf16 v[120:123], v[164:167], v[190:193], v[120:123]
	v_mfma_f32_16x16x32_bf16 v[116:119], v[172:175], v[190:193], v[116:119]
	v_mfma_f32_16x16x32_bf16 v[104:107], v[164:167], v[216:219], v[104:107]
	v_mfma_f32_16x16x32_bf16 v[100:103], v[172:175], v[216:219], v[100:103]
	v_mfma_f32_16x16x32_bf16 v[88:91], v[164:167], v[228:231], v[88:91]
	v_mfma_f32_16x16x32_bf16 v[84:87], v[172:175], v[228:231], v[84:87]
	v_mfma_f32_16x16x32_bf16 v[72:75], v[164:167], v[236:239], v[72:75]
	v_mfma_f32_16x16x32_bf16 v[68:71], v[172:175], v[236:239], v[68:71]
	s_setprio 0
	s_setprio 1
	v_mfma_f32_16x16x32_bf16 v[120:123], v[168:171], v[212:215], v[120:123]
	v_mfma_f32_16x16x32_bf16 v[116:119], v[182:185], v[212:215], v[116:119]
	v_mfma_f32_16x16x32_bf16 v[104:107], v[168:171], v[224:227], v[104:107]
	v_mfma_f32_16x16x32_bf16 v[100:103], v[182:185], v[224:227], v[100:103]
	v_mfma_f32_16x16x32_bf16 v[88:91], v[168:171], v[232:235], v[88:91]
	v_mfma_f32_16x16x32_bf16 v[84:87], v[182:185], v[232:235], v[84:87]
	v_mfma_f32_16x16x32_bf16 v[72:75], v[168:171], v[240:243], v[72:75]
	v_mfma_f32_16x16x32_bf16 v[68:71], v[182:185], v[240:243], v[68:71]
	s_setprio 0
	s_barrier
	s_add_i32 s2, s2, s15
	v_lshl_add_u64 v[176:177], v[176:177], 0, s[30:31]
	s_mov_b32 m0, s2
	ds_read_b128 v[190:193], v181 offset:49152
	ds_read_b128 v[212:215], v181 offset:50176
	ds_read_b128 v[216:219], v181 offset:51200
	ds_read_b128 v[224:227], v181 offset:52224
	ds_read_b128 v[228:231], v181 offset:53248
	ds_read_b128 v[232:235], v181 offset:54272
	ds_read_b128 v[236:239], v181 offset:55296
	ds_read_b128 v[240:243], v181 offset:56320
	global_load_lds_dwordx4 v[176:177], off
	s_add_i32 m0, s2, 0x2000
	s_add_u32 s2, s36, 0x80080
	v_lshl_add_u64 v[176:177], v[186:187], 0, s[30:31]
	s_addc_u32 s3, s37, 0
	s_add_i32 s36, s46, s15
	global_load_lds_dwordx4 v[176:177], off
	v_lshl_add_u64 v[176:177], s[2:3], 0, v[132:133]
	s_mov_b32 m0, s36
	s_nop 0
	global_load_lds_dwordx4 v[176:177], off
	v_lshl_add_u64 v[176:177], s[2:3], 0, v[134:135]
	s_add_i32 m0, s36, 0x2000
	s_nop 0
	global_load_lds_dwordx4 v[176:177], off
	v_lshl_add_u64 v[176:177], v[194:195], 0, s[30:31]
	s_mov_b32 m0, s22
	s_nop 0
	global_load_lds_dwordx4 v[176:177], off
	v_lshl_add_u64 v[176:177], v[244:245], 0, s[30:31]
	s_mov_b32 m0, s23
	s_nop 0
	global_load_lds_dwordx4 v[176:177], off
	s_waitcnt vmcnt(8)
	s_waitcnt lgkmcnt(0)
	s_barrier
	s_setprio 1
	s_waitcnt lgkmcnt(0)
	v_mfma_f32_16x16x32_bf16 v[64:67], v[148:151], v[190:193], v[64:67]
	v_mfma_f32_16x16x32_bf16 v[60:63], v[156:159], v[190:193], v[60:63]
	v_mfma_f32_16x16x32_bf16 v[48:51], v[148:151], v[216:219], v[48:51]
	v_mfma_f32_16x16x32_bf16 v[44:47], v[156:159], v[216:219], v[44:47]
	v_mfma_f32_16x16x32_bf16 v[32:35], v[148:151], v[228:231], v[32:35]
	v_mfma_f32_16x16x32_bf16 v[28:31], v[156:159], v[228:231], v[28:31]
	v_mfma_f32_16x16x32_bf16 v[16:19], v[148:151], v[236:239], v[16:19]
	v_mfma_f32_16x16x32_bf16 v[4:7], v[156:159], v[236:239], v[4:7]
	s_setprio 0
	s_setprio 1
	v_mfma_f32_16x16x32_bf16 v[64:67], v[152:155], v[212:215], v[64:67]
	v_mfma_f32_16x16x32_bf16 v[60:63], v[160:163], v[212:215], v[60:63]
	v_mfma_f32_16x16x32_bf16 v[48:51], v[152:155], v[224:227], v[48:51]
	v_mfma_f32_16x16x32_bf16 v[44:47], v[160:163], v[224:227], v[44:47]
	v_mfma_f32_16x16x32_bf16 v[32:35], v[152:155], v[232:235], v[32:35]
	v_mfma_f32_16x16x32_bf16 v[28:31], v[160:163], v[232:235], v[28:31]
	v_mfma_f32_16x16x32_bf16 v[16:19], v[152:155], v[240:243], v[16:19]
	v_mfma_f32_16x16x32_bf16 v[4:7], v[160:163], v[240:243], v[4:7]
	s_setprio 0
	s_setprio 1
	v_mfma_f32_16x16x32_bf16 v[52:55], v[164:167], v[190:193], v[52:55]
	v_mfma_f32_16x16x32_bf16 v[56:59], v[172:175], v[190:193], v[56:59]
	v_mfma_f32_16x16x32_bf16 v[36:39], v[164:167], v[216:219], v[36:39]
	v_mfma_f32_16x16x32_bf16 v[40:43], v[172:175], v[216:219], v[40:43]
	v_mfma_f32_16x16x32_bf16 v[20:23], v[164:167], v[228:231], v[20:23]
	v_mfma_f32_16x16x32_bf16 v[24:27], v[172:175], v[228:231], v[24:27]
	v_mfma_f32_16x16x32_bf16 v[8:11], v[164:167], v[236:239], v[8:11]
	v_mfma_f32_16x16x32_bf16 v[12:15], v[172:175], v[236:239], v[12:15]
	s_setprio 0
	s_setprio 1
	v_mfma_f32_16x16x32_bf16 v[52:55], v[168:171], v[212:215], v[52:55]
	v_mfma_f32_16x16x32_bf16 v[56:59], v[182:185], v[212:215], v[56:59]
	v_mfma_f32_16x16x32_bf16 v[36:39], v[168:171], v[224:227], v[36:39]
	v_mfma_f32_16x16x32_bf16 v[40:43], v[182:185], v[224:227], v[40:43]
	v_mfma_f32_16x16x32_bf16 v[20:23], v[168:171], v[232:235], v[20:23]
	v_mfma_f32_16x16x32_bf16 v[24:27], v[182:185], v[232:235], v[24:27]
	v_mfma_f32_16x16x32_bf16 v[8:11], v[168:171], v[240:243], v[8:11]
	v_mfma_f32_16x16x32_bf16 v[12:15], v[182:185], v[240:243], v[12:15]
	s_setprio 0
	s_barrier
	s_add_i32 s45, s45, 2
	s_add_u32 s34, s34, 0x100
	s_addc_u32 s35, s35, 0
	s_add_u32 s42, s42, 0x100
	s_addc_u32 s43, s43, 0
	s_cmp_gt_u32 s45, 29
	s_cbranch_scc0 .LBB0_477
	s_and_b64 vcc, exec, s[76:77]
	s_cbranch_vccz .LBB0_480
	s_barrier

.LBB0_991:
	s_add_u32 s2, s0, 0x80
	s_addc_u32 s3, s1, 0
	s_cmp_eq_u32 s57, 4
	s_cselect_b32 s37, s53, s3
	s_cselect_b32 s36, s52, s2
	s_cselect_b32 s35, s55, s56
	s_cselect_b32 s34, s54, s29
	s_add_i32 s2, 0, 0x10000
	v_add_u32_e32 v2, s2, v168
	s_add_i32 s58, 0, 0x14000
	ds_read_b128 v[148:151], v2
	ds_read_b128 v[152:155], v2 offset:1024
	ds_read_b128 v[156:159], v2 offset:2048
	ds_read_b128 v[160:163], v2 offset:3072
	v_add_u32_e32 v2, s58, v168
	ds_read_b128 v[170:173], v2
	ds_read_b128 v[174:177], v2 offset:1024
	ds_read_b128 v[178:181], v2 offset:2048
	ds_read_b128 v[182:185], v2 offset:3072
	v_lshl_add_u64 v[164:165], s[0:1], 0, v[144:145]
	s_add_i32 m0, s18, 0xc000
	ds_read_b128 v[190:193], v169
	ds_read_b128 v[212:215], v169 offset:1024
	ds_read_b128 v[216:219], v169 offset:2048
	ds_read_b128 v[224:227], v169 offset:3072
	ds_read_b128 v[228:231], v169 offset:4096
	ds_read_b128 v[232:235], v169 offset:5120
	ds_read_b128 v[236:239], v169 offset:6144
	ds_read_b128 v[240:243], v169 offset:7168
	global_load_lds_dwordx4 v[164:165], off
	v_lshl_add_u64 v[164:165], s[0:1], 0, v[146:147]
	s_add_i32 m0, s18, 0xe000
	s_nop 0
	global_load_lds_dwordx4 v[164:165], off
	s_waitcnt vmcnt(8)
	s_waitcnt lgkmcnt(0)
	s_barrier
	s_setprio 1
	s_waitcnt lgkmcnt(0)
	v_mfma_f32_16x16x32_bf16 v[128:131], v[148:151], v[190:193], v[128:131]
	v_mfma_f32_16x16x32_bf16 v[124:127], v[156:159], v[190:193], v[124:127]
	v_mfma_f32_16x16x32_bf16 v[112:115], v[148:151], v[216:219], v[112:115]
	v_mfma_f32_16x16x32_bf16 v[108:111], v[156:159], v[216:219], v[108:111]
	v_mfma_f32_16x16x32_bf16 v[96:99], v[148:151], v[228:231], v[96:99]
	v_mfma_f32_16x16x32_bf16 v[92:95], v[156:159], v[228:231], v[92:95]
	v_mfma_f32_16x16x32_bf16 v[80:83], v[148:151], v[236:239], v[80:83]
	v_mfma_f32_16x16x32_bf16 v[76:79], v[156:159], v[236:239], v[76:79]
	s_setprio 0
	s_setprio 1
	v_mfma_f32_16x16x32_bf16 v[128:131], v[152:155], v[212:215], v[128:131]
	v_mfma_f32_16x16x32_bf16 v[124:127], v[160:163], v[212:215], v[124:127]
	v_mfma_f32_16x16x32_bf16 v[112:115], v[152:155], v[224:227], v[112:115]
	v_mfma_f32_16x16x32_bf16 v[108:111], v[160:163], v[224:227], v[108:111]
	v_mfma_f32_16x16x32_bf16 v[96:99], v[152:155], v[232:235], v[96:99]
	v_mfma_f32_16x16x32_bf16 v[92:95], v[160:163], v[232:235], v[92:95]
	v_mfma_f32_16x16x32_bf16 v[80:83], v[152:155], v[240:243], v[80:83]
	v_mfma_f32_16x16x32_bf16 v[76:79], v[160:163], v[240:243], v[76:79]
	s_setprio 0
	s_setprio 1
	v_mfma_f32_16x16x32_bf16 v[120:123], v[170:173], v[190:193], v[120:123]
	v_mfma_f32_16x16x32_bf16 v[116:119], v[178:181], v[190:193], v[116:119]
	v_mfma_f32_16x16x32_bf16 v[104:107], v[170:173], v[216:219], v[104:107]
	v_mfma_f32_16x16x32_bf16 v[100:103], v[178:181], v[216:219], v[100:103]
	v_mfma_f32_16x16x32_bf16 v[88:91], v[170:173], v[228:231], v[88:91]
	v_mfma_f32_16x16x32_bf16 v[84:87], v[178:181], v[228:231], v[84:87]
	v_mfma_f32_16x16x32_bf16 v[72:75], v[170:173], v[236:239], v[72:75]
	v_mfma_f32_16x16x32_bf16 v[68:71], v[178:181], v[236:239], v[68:71]
	s_setprio 0
	s_setprio 1
	v_mfma_f32_16x16x32_bf16 v[120:123], v[174:177], v[212:215], v[120:123]
	v_mfma_f32_16x16x32_bf16 v[116:119], v[182:185], v[212:215], v[116:119]
	v_mfma_f32_16x16x32_bf16 v[104:107], v[174:177], v[224:227], v[104:107]
	v_mfma_f32_16x16x32_bf16 v[100:103], v[182:185], v[224:227], v[100:103]
	v_mfma_f32_16x16x32_bf16 v[88:91], v[174:177], v[232:235], v[88:91]
	v_mfma_f32_16x16x32_bf16 v[84:87], v[182:185], v[232:235], v[84:87]
	v_mfma_f32_16x16x32_bf16 v[72:75], v[174:177], v[240:243], v[72:75]
	v_mfma_f32_16x16x32_bf16 v[68:71], v[182:185], v[240:243], v[68:71]
	s_setprio 0
	s_barrier
	s_add_i32 s2, s2, s17
	v_lshl_add_u64 v[164:165], s[34:35], 0, v[132:133]
	s_mov_b32 m0, s2
	ds_read_b128 v[190:193], v169 offset:16384
	ds_read_b128 v[212:215], v169 offset:17408
	ds_read_b128 v[216:219], v169 offset:18432
	ds_read_b128 v[224:227], v169 offset:19456
	ds_read_b128 v[228:231], v169 offset:20480
	ds_read_b128 v[232:235], v169 offset:21504
	ds_read_b128 v[236:239], v169 offset:22528
	ds_read_b128 v[240:243], v169 offset:23552
	global_load_lds_dwordx4 v[164:165], off
	s_add_i32 m0, s2, 0x2000
	s_add_u32 s2, s34, 0x20000
	v_lshl_add_u64 v[186:187], s[34:35], 0, v[134:135]
	s_addc_u32 s3, s35, 0
	s_add_i32 s58, s58, s17
	global_load_lds_dwordx4 v[186:187], off
	v_lshl_add_u64 v[194:195], s[2:3], 0, v[132:133]
	s_mov_b32 m0, s58
	v_lshl_add_u64 v[244:245], s[36:37], 0, v[138:139]
	global_load_lds_dwordx4 v[194:195], off
	v_lshl_add_u64 v[194:195], s[2:3], 0, v[134:135]
	s_add_i32 m0, s58, 0x2000
	s_nop 0
	global_load_lds_dwordx4 v[194:195], off
	v_lshl_add_u64 v[194:195], s[36:37], 0, v[136:137]
	s_mov_b32 m0, s18
	s_nop 0
	global_load_lds_dwordx4 v[194:195], off
	s_mov_b32 m0, s19
	s_nop 0
	global_load_lds_dwordx4 v[244:245], off
	s_waitcnt vmcnt(8)
	s_waitcnt lgkmcnt(0)
	s_barrier
	s_setprio 1
	s_waitcnt lgkmcnt(0)
	v_mfma_f32_16x16x32_bf16 v[64:67], v[148:151], v[190:193], v[64:67]
	v_mfma_f32_16x16x32_bf16 v[60:63], v[156:159], v[190:193], v[60:63]
	v_mfma_f32_16x16x32_bf16 v[48:51], v[148:151], v[216:219], v[48:51]
	v_mfma_f32_16x16x32_bf16 v[44:47], v[156:159], v[216:219], v[44:47]
	v_mfma_f32_16x16x32_bf16 v[32:35], v[148:151], v[228:231], v[32:35]
	v_mfma_f32_16x16x32_bf16 v[28:31], v[156:159], v[228:231], v[28:31]
	v_mfma_f32_16x16x32_bf16 v[16:19], v[148:151], v[236:239], v[16:19]
	v_mfma_f32_16x16x32_bf16 v[12:15], v[156:159], v[236:239], v[12:15]
	s_setprio 0
	s_setprio 1
	v_mfma_f32_16x16x32_bf16 v[64:67], v[152:155], v[212:215], v[64:67]
	v_mfma_f32_16x16x32_bf16 v[60:63], v[160:163], v[212:215], v[60:63]
	v_mfma_f32_16x16x32_bf16 v[48:51], v[152:155], v[224:227], v[48:51]
	v_mfma_f32_16x16x32_bf16 v[44:47], v[160:163], v[224:227], v[44:47]
	v_mfma_f32_16x16x32_bf16 v[32:35], v[152:155], v[232:235], v[32:35]
	v_mfma_f32_16x16x32_bf16 v[28:31], v[160:163], v[232:235], v[28:31]
	v_mfma_f32_16x16x32_bf16 v[16:19], v[152:155], v[240:243], v[16:19]
	v_mfma_f32_16x16x32_bf16 v[12:15], v[160:163], v[240:243], v[12:15]
	s_setprio 0
	s_setprio 1
	v_mfma_f32_16x16x32_bf16 v[52:55], v[170:173], v[190:193], v[52:55]
	v_mfma_f32_16x16x32_bf16 v[56:59], v[178:181], v[190:193], v[56:59]
	v_mfma_f32_16x16x32_bf16 v[36:39], v[170:173], v[216:219], v[36:39]
	v_mfma_f32_16x16x32_bf16 v[40:43], v[178:181], v[216:219], v[40:43]
	v_mfma_f32_16x16x32_bf16 v[20:23], v[170:173], v[228:231], v[20:23]
	v_mfma_f32_16x16x32_bf16 v[24:27], v[178:181], v[228:231], v[24:27]
	v_mfma_f32_16x16x32_bf16 v[4:7], v[170:173], v[236:239], v[4:7]
	v_mfma_f32_16x16x32_bf16 v[8:11], v[178:181], v[236:239], v[8:11]
	s_setprio 0
	s_setprio 1
	v_mfma_f32_16x16x32_bf16 v[52:55], v[174:177], v[212:215], v[52:55]
	v_mfma_f32_16x16x32_bf16 v[56:59], v[182:185], v[212:215], v[56:59]
	v_mfma_f32_16x16x32_bf16 v[36:39], v[174:177], v[224:227], v[36:39]
	v_mfma_f32_16x16x32_bf16 v[40:43], v[182:185], v[224:227], v[40:43]
	v_mfma_f32_16x16x32_bf16 v[20:23], v[174:177], v[232:235], v[20:23]
	v_mfma_f32_16x16x32_bf16 v[24:27], v[182:185], v[232:235], v[24:27]
	v_mfma_f32_16x16x32_bf16 v[4:7], v[174:177], v[240:243], v[4:7]
	v_mfma_f32_16x16x32_bf16 v[8:11], v[182:185], v[240:243], v[8:11]
	s_setprio 0
	s_barrier
	s_add_i32 s2, 0, 0x18000
	v_add_u32_e32 v2, s2, v168
	s_add_i32 s58, 0, 0x1c000
	ds_read_b128 v[148:151], v2
	ds_read_b128 v[152:155], v2 offset:1024
	ds_read_b128 v[156:159], v2 offset:2048
	ds_read_b128 v[160:163], v2 offset:3072
	v_add_u32_e32 v2, s58, v168
	ds_read_b128 v[170:173], v2
	ds_read_b128 v[174:177], v2 offset:1024
	ds_read_b128 v[178:181], v2 offset:2048
	ds_read_b128 v[182:185], v2 offset:3072
	s_mov_b32 m0, s20
	v_lshl_add_u64 v[246:247], s[36:37], 0, v[140:141]
	ds_read_b128 v[190:193], v169 offset:32768
	ds_read_b128 v[212:215], v169 offset:33792
	ds_read_b128 v[216:219], v169 offset:34816
	ds_read_b128 v[224:227], v169 offset:35840
	ds_read_b128 v[228:231], v169 offset:36864
	ds_read_b128 v[232:235], v169 offset:37888
	ds_read_b128 v[236:239], v169 offset:38912
	ds_read_b128 v[240:243], v169 offset:39936
	global_load_lds_dwordx4 v[246:247], off
	v_lshl_add_u64 v[246:247], s[36:37], 0, v[142:143]
	s_mov_b32 m0, s21
	s_nop 0
	global_load_lds_dwordx4 v[246:247], off
	s_waitcnt vmcnt(8)
	s_waitcnt lgkmcnt(0)
	s_barrier
	s_setprio 1
	s_waitcnt lgkmcnt(0)
	v_mfma_f32_16x16x32_bf16 v[128:131], v[148:151], v[190:193], v[128:131]
	v_mfma_f32_16x16x32_bf16 v[124:127], v[156:159], v[190:193], v[124:127]
	v_mfma_f32_16x16x32_bf16 v[112:115], v[148:151], v[216:219], v[112:115]
	v_mfma_f32_16x16x32_bf16 v[108:111], v[156:159], v[216:219], v[108:111]
	v_mfma_f32_16x16x32_bf16 v[96:99], v[148:151], v[228:231], v[96:99]
	v_mfma_f32_16x16x32_bf16 v[92:95], v[156:159], v[228:231], v[92:95]
	v_mfma_f32_16x16x32_bf16 v[80:83], v[148:151], v[236:239], v[80:83]
	v_mfma_f32_16x16x32_bf16 v[76:79], v[156:159], v[236:239], v[76:79]
	s_setprio 0
	s_setprio 1
	v_mfma_f32_16x16x32_bf16 v[128:131], v[152:155], v[212:215], v[128:131]
	v_mfma_f32_16x16x32_bf16 v[124:127], v[160:163], v[212:215], v[124:127]
	v_mfma_f32_16x16x32_bf16 v[112:115], v[152:155], v[224:227], v[112:115]
	v_mfma_f32_16x16x32_bf16 v[108:111], v[160:163], v[224:227], v[108:111]
	v_mfma_f32_16x16x32_bf16 v[96:99], v[152:155], v[232:235], v[96:99]
	v_mfma_f32_16x16x32_bf16 v[92:95], v[160:163], v[232:235], v[92:95]
	v_mfma_f32_16x16x32_bf16 v[80:83], v[152:155], v[240:243], v[80:83]
	v_mfma_f32_16x16x32_bf16 v[76:79], v[160:163], v[240:243], v[76:79]
	s_setprio 0
	s_setprio 1
	v_mfma_f32_16x16x32_bf16 v[120:123], v[170:173], v[190:193], v[120:123]
	v_mfma_f32_16x16x32_bf16 v[116:119], v[178:181], v[190:193], v[116:119]
	v_mfma_f32_16x16x32_bf16 v[104:107], v[170:173], v[216:219], v[104:107]
	v_mfma_f32_16x16x32_bf16 v[100:103], v[178:181], v[216:219], v[100:103]
	v_mfma_f32_16x16x32_bf16 v[88:91], v[170:173], v[228:231], v[88:91]
	v_mfma_f32_16x16x32_bf16 v[84:87], v[178:181], v[228:231], v[84:87]
	v_mfma_f32_16x16x32_bf16 v[72:75], v[170:173], v[236:239], v[72:75]
	v_mfma_f32_16x16x32_bf16 v[68:71], v[178:181], v[236:239], v[68:71]
	s_setprio 0
	s_setprio 1
	v_mfma_f32_16x16x32_bf16 v[120:123], v[174:177], v[212:215], v[120:123]
	v_mfma_f32_16x16x32_bf16 v[116:119], v[182:185], v[212:215], v[116:119]
	v_mfma_f32_16x16x32_bf16 v[104:107], v[174:177], v[224:227], v[104:107]
	v_mfma_f32_16x16x32_bf16 v[100:103], v[182:185], v[224:227], v[100:103]
	v_mfma_f32_16x16x32_bf16 v[88:91], v[174:177], v[232:235], v[88:91]
	v_mfma_f32_16x16x32_bf16 v[84:87], v[182:185], v[232:235], v[84:87]
	v_mfma_f32_16x16x32_bf16 v[72:75], v[174:177], v[240:243], v[72:75]
	v_mfma_f32_16x16x32_bf16 v[68:71], v[182:185], v[240:243], v[68:71]
	s_setprio 0
	s_barrier
	s_add_i32 s2, s2, s17
	v_lshl_add_u64 v[164:165], v[164:165], 0, s[30:31]
	s_mov_b32 m0, s2
	ds_read_b128 v[190:193], v169 offset:49152
	ds_read_b128 v[212:215], v169 offset:50176
	ds_read_b128 v[216:219], v169 offset:51200
	ds_read_b128 v[224:227], v169 offset:52224
	ds_read_b128 v[228:231], v169 offset:53248
	ds_read_b128 v[232:235], v169 offset:54272
	ds_read_b128 v[236:239], v169 offset:55296
	ds_read_b128 v[240:243], v169 offset:56320
	global_load_lds_dwordx4 v[164:165], off
	s_add_i32 m0, s2, 0x2000
	s_add_u32 s2, s34, 0x20080
	v_lshl_add_u64 v[164:165], v[186:187], 0, s[30:31]
	s_addc_u32 s3, s35, 0
	s_add_i32 s34, s58, s17
	global_load_lds_dwordx4 v[164:165], off
	v_lshl_add_u64 v[164:165], s[2:3], 0, v[132:133]
	s_mov_b32 m0, s34
	s_nop 0
	global_load_lds_dwordx4 v[164:165], off
	v_lshl_add_u64 v[164:165], s[2:3], 0, v[134:135]
	s_add_i32 m0, s34, 0x2000
	s_nop 0
	global_load_lds_dwordx4 v[164:165], off
	v_lshl_add_u64 v[164:165], v[194:195], 0, s[30:31]
	s_mov_b32 m0, s24
	s_nop 0
	global_load_lds_dwordx4 v[164:165], off
	v_lshl_add_u64 v[164:165], v[244:245], 0, s[30:31]
	s_mov_b32 m0, s25
	s_nop 0
	global_load_lds_dwordx4 v[164:165], off
	s_waitcnt vmcnt(8)
	s_waitcnt lgkmcnt(0)
	s_barrier
	s_setprio 1
	s_waitcnt lgkmcnt(0)
	v_mfma_f32_16x16x32_bf16 v[64:67], v[148:151], v[190:193], v[64:67]
	v_mfma_f32_16x16x32_bf16 v[60:63], v[156:159], v[190:193], v[60:63]
	v_mfma_f32_16x16x32_bf16 v[48:51], v[148:151], v[216:219], v[48:51]
	v_mfma_f32_16x16x32_bf16 v[44:47], v[156:159], v[216:219], v[44:47]
	v_mfma_f32_16x16x32_bf16 v[32:35], v[148:151], v[228:231], v[32:35]
	v_mfma_f32_16x16x32_bf16 v[28:31], v[156:159], v[228:231], v[28:31]
	v_mfma_f32_16x16x32_bf16 v[16:19], v[148:151], v[236:239], v[16:19]
	v_mfma_f32_16x16x32_bf16 v[12:15], v[156:159], v[236:239], v[12:15]
	s_setprio 0
	s_setprio 1
	v_mfma_f32_16x16x32_bf16 v[64:67], v[152:155], v[212:215], v[64:67]
	v_mfma_f32_16x16x32_bf16 v[60:63], v[160:163], v[212:215], v[60:63]
	v_mfma_f32_16x16x32_bf16 v[48:51], v[152:155], v[224:227], v[48:51]
	v_mfma_f32_16x16x32_bf16 v[44:47], v[160:163], v[224:227], v[44:47]
	v_mfma_f32_16x16x32_bf16 v[32:35], v[152:155], v[232:235], v[32:35]
	v_mfma_f32_16x16x32_bf16 v[28:31], v[160:163], v[232:235], v[28:31]
	v_mfma_f32_16x16x32_bf16 v[16:19], v[152:155], v[240:243], v[16:19]
	v_mfma_f32_16x16x32_bf16 v[12:15], v[160:163], v[240:243], v[12:15]
	s_setprio 0
	s_setprio 1
	v_mfma_f32_16x16x32_bf16 v[52:55], v[170:173], v[190:193], v[52:55]
	v_mfma_f32_16x16x32_bf16 v[56:59], v[178:181], v[190:193], v[56:59]
	v_mfma_f32_16x16x32_bf16 v[36:39], v[170:173], v[216:219], v[36:39]
	v_mfma_f32_16x16x32_bf16 v[40:43], v[178:181], v[216:219], v[40:43]
	v_mfma_f32_16x16x32_bf16 v[20:23], v[170:173], v[228:231], v[20:23]
	v_mfma_f32_16x16x32_bf16 v[24:27], v[178:181], v[228:231], v[24:27]
	v_mfma_f32_16x16x32_bf16 v[4:7], v[170:173], v[236:239], v[4:7]
	v_mfma_f32_16x16x32_bf16 v[8:11], v[178:181], v[236:239], v[8:11]
	s_setprio 0
	s_setprio 1
	v_mfma_f32_16x16x32_bf16 v[52:55], v[174:177], v[212:215], v[52:55]
	v_mfma_f32_16x16x32_bf16 v[56:59], v[182:185], v[212:215], v[56:59]
	v_mfma_f32_16x16x32_bf16 v[36:39], v[174:177], v[224:227], v[36:39]
	v_mfma_f32_16x16x32_bf16 v[40:43], v[182:185], v[224:227], v[40:43]
	v_mfma_f32_16x16x32_bf16 v[20:23], v[174:177], v[232:235], v[20:23]
	v_mfma_f32_16x16x32_bf16 v[24:27], v[182:185], v[232:235], v[24:27]
	v_mfma_f32_16x16x32_bf16 v[4:7], v[174:177], v[240:243], v[4:7]
	v_mfma_f32_16x16x32_bf16 v[8:11], v[182:185], v[240:243], v[8:11]
	s_setprio 0
	s_barrier
	s_add_i32 s57, s57, 2
	s_add_u32 s0, s0, 0x100
	s_addc_u32 s1, s1, 0
	s_add_u32 s29, s29, 0x100
	s_addc_u32 s56, s56, 0
	s_cmp_gt_u32 s57, 5
	s_cbranch_scc0 .LBB0_991
	s_and_b64 vcc, exec, s[42:43]
	s_cbranch_vccz .LBB0_994
	s_barrier

.LBB0_1105:
	s_add_u32 s62, s34, s7
	s_addc_u32 s63, s35, 0
	s_add_u32 s56, s62, 0x100
	s_addc_u32 s57, s63, 0
	s_and_b64 s[2:3], s[54:55], exec
	s_cselect_b32 s56, s44, s56
	s_cselect_b32 s57, s45, s57
	s_add_u32 s2, s50, s7
	s_addc_u32 s3, s51, 0
	s_add_u32 s7, s2, 0x100
	s_addc_u32 s58, s3, 0
	s_and_b64 s[2:3], s[54:55], exec
	s_cselect_b32 s59, s49, s58
	s_cselect_b32 s58, s48, s7
	s_add_i32 s55, 0, 0x10000
	s_add_i32 s69, 0, 0x14000
	v_add_u32_e32 v2, s55, v152
	s_add_i32 s68, s55, s17
	ds_read_b128 v[132:135], v2
	ds_read_b128 v[154:157], v2 offset:1024
	ds_read_b128 v[158:161], v2 offset:2048
	ds_read_b128 v[162:165], v2 offset:3072
	v_add_u32_e32 v2, s69, v152
	s_add_i32 m0, s18, 0xc000
	s_add_i32 s71, s18, 0xe000
	s_add_i32 s65, s68, 0x2000
	ds_read_b128 v[166:169], v2
	ds_read_b128 v[170:173], v2 offset:1024
	ds_read_b128 v[174:177], v2 offset:2048
	ds_read_b128 v[178:181], v2 offset:3072
	s_add_u32 s60, s58, 0x10000
	s_addc_u32 s61, s59, 0
	s_add_i32 s3, 0, 0x18000
	s_add_i32 s67, s69, s17
	s_add_i32 s64, s3, s17
	s_add_i32 s66, s67, 0x2000
	s_add_i32 s2, 0, 0x1c000
	s_add_i32 s7, s64, 0x2000
	s_add_u32 s54, s58, 0x10080
	s_addc_u32 s55, s59, 0
	s_add_i32 s70, s2, s17
	s_add_i32 s69, s70, 0x2000
	v_lshl_add_u64 v[148:149], s[62:63], 0, v[144:145]
	v_lshl_add_u64 v[148:149], v[148:149], 0, s[30:31]
	ds_read_b128 v[182:185], v153
	ds_read_b128 v[190:193], v153 offset:1024
	ds_read_b128 v[212:215], v153 offset:2048
	ds_read_b128 v[216:219], v153 offset:3072
	ds_read_b128 v[224:227], v153 offset:4096
	ds_read_b128 v[228:231], v153 offset:5120
	ds_read_b128 v[232:235], v153 offset:6144
	ds_read_b128 v[236:239], v153 offset:7168
	global_load_lds_dwordx4 v[148:149], off
	v_lshl_add_u64 v[148:149], s[62:63], 0, v[146:147]
	v_lshl_add_u64 v[148:149], v[148:149], 0, s[30:31]
	s_mov_b32 m0, s71
	s_nop 0
	global_load_lds_dwordx4 v[148:149], off
	s_waitcnt vmcnt(8)
	s_waitcnt lgkmcnt(0)
	s_barrier
	s_setprio 1
	s_waitcnt lgkmcnt(0)
	v_mfma_f32_16x16x32_bf16 v[128:131], v[132:135], v[182:185], v[128:131]
	v_mfma_f32_16x16x32_bf16 v[124:127], v[158:161], v[182:185], v[124:127]
	v_mfma_f32_16x16x32_bf16 v[112:115], v[132:135], v[212:215], v[112:115]
	v_mfma_f32_16x16x32_bf16 v[108:111], v[158:161], v[212:215], v[108:111]
	v_mfma_f32_16x16x32_bf16 v[96:99], v[132:135], v[224:227], v[96:99]
	v_mfma_f32_16x16x32_bf16 v[92:95], v[158:161], v[224:227], v[92:95]
	v_mfma_f32_16x16x32_bf16 v[80:83], v[132:135], v[232:235], v[80:83]
	v_mfma_f32_16x16x32_bf16 v[76:79], v[158:161], v[232:235], v[76:79]
	s_setprio 0
	s_setprio 1
	v_mfma_f32_16x16x32_bf16 v[128:131], v[154:157], v[190:193], v[128:131]
	v_mfma_f32_16x16x32_bf16 v[124:127], v[162:165], v[190:193], v[124:127]
	v_mfma_f32_16x16x32_bf16 v[112:115], v[154:157], v[216:219], v[112:115]
	v_mfma_f32_16x16x32_bf16 v[108:111], v[162:165], v[216:219], v[108:111]
	v_mfma_f32_16x16x32_bf16 v[96:99], v[154:157], v[228:231], v[96:99]
	v_mfma_f32_16x16x32_bf16 v[92:95], v[162:165], v[228:231], v[92:95]
	v_mfma_f32_16x16x32_bf16 v[80:83], v[154:157], v[236:239], v[80:83]
	v_mfma_f32_16x16x32_bf16 v[76:79], v[162:165], v[236:239], v[76:79]
	s_setprio 0
	s_setprio 1
	v_mfma_f32_16x16x32_bf16 v[120:123], v[166:169], v[182:185], v[120:123]
	v_mfma_f32_16x16x32_bf16 v[116:119], v[174:177], v[182:185], v[116:119]
	v_mfma_f32_16x16x32_bf16 v[104:107], v[166:169], v[212:215], v[104:107]
	v_mfma_f32_16x16x32_bf16 v[100:103], v[174:177], v[212:215], v[100:103]
	v_mfma_f32_16x16x32_bf16 v[88:91], v[166:169], v[224:227], v[88:91]
	v_mfma_f32_16x16x32_bf16 v[84:87], v[174:177], v[224:227], v[84:87]
	v_mfma_f32_16x16x32_bf16 v[72:75], v[166:169], v[232:235], v[72:75]
	v_mfma_f32_16x16x32_bf16 v[68:71], v[174:177], v[232:235], v[68:71]
	s_setprio 0
	s_setprio 1
	v_mfma_f32_16x16x32_bf16 v[120:123], v[170:173], v[190:193], v[120:123]
	v_mfma_f32_16x16x32_bf16 v[116:119], v[178:181], v[190:193], v[116:119]
	v_mfma_f32_16x16x32_bf16 v[104:107], v[170:173], v[216:219], v[104:107]
	v_mfma_f32_16x16x32_bf16 v[100:103], v[178:181], v[216:219], v[100:103]
	v_mfma_f32_16x16x32_bf16 v[88:91], v[170:173], v[228:231], v[88:91]
	v_mfma_f32_16x16x32_bf16 v[84:87], v[178:181], v[228:231], v[84:87]
	v_mfma_f32_16x16x32_bf16 v[72:75], v[170:173], v[236:239], v[72:75]
	v_mfma_f32_16x16x32_bf16 v[68:71], v[178:181], v[236:239], v[68:71]
	s_setprio 0
	s_barrier
	s_mov_b32 m0, s68
	v_lshl_add_u64 v[148:149], s[58:59], 0, v[136:137]
	ds_read_b128 v[182:185], v153 offset:16384
	ds_read_b128 v[190:193], v153 offset:17408
	ds_read_b128 v[212:215], v153 offset:18432
	ds_read_b128 v[216:219], v153 offset:19456
	ds_read_b128 v[224:227], v153 offset:20480
	ds_read_b128 v[228:231], v153 offset:21504
	ds_read_b128 v[232:235], v153 offset:22528
	ds_read_b128 v[236:239], v153 offset:23552
	global_load_lds_dwordx4 v[148:149], off
	v_lshl_add_u64 v[186:187], s[58:59], 0, v[138:139]
	s_mov_b32 m0, s65
	v_lshl_add_u64 v[194:195], s[60:61], 0, v[136:137]
	global_load_lds_dwordx4 v[186:187], off
	s_mov_b32 m0, s67
	v_lshl_add_u64 v[240:241], s[56:57], 0, v[142:143]
	global_load_lds_dwordx4 v[194:195], off
	v_lshl_add_u64 v[194:195], s[60:61], 0, v[138:139]
	s_mov_b32 m0, s66
	s_nop 0
	global_load_lds_dwordx4 v[194:195], off
	v_lshl_add_u64 v[194:195], s[56:57], 0, v[140:141]
	s_mov_b32 m0, s18
	s_nop 0
	global_load_lds_dwordx4 v[194:195], off
	s_mov_b32 m0, s19
	s_nop 0
	global_load_lds_dwordx4 v[240:241], off
	s_waitcnt vmcnt(8)
	s_waitcnt lgkmcnt(0)
	s_barrier
	s_setprio 1
	s_waitcnt lgkmcnt(0)
	v_mfma_f32_16x16x32_bf16 v[56:59], v[132:135], v[182:185], v[56:59]
	v_mfma_f32_16x16x32_bf16 v[52:55], v[158:161], v[182:185], v[52:55]
	v_mfma_f32_16x16x32_bf16 v[40:43], v[132:135], v[212:215], v[40:43]
	v_mfma_f32_16x16x32_bf16 v[36:39], v[158:161], v[212:215], v[36:39]
	v_mfma_f32_16x16x32_bf16 v[24:27], v[132:135], v[224:227], v[24:27]
	v_mfma_f32_16x16x32_bf16 v[20:23], v[158:161], v[224:227], v[20:23]
	v_mfma_f32_16x16x32_bf16 v[8:11], v[132:135], v[232:235], v[8:11]
	v_mfma_f32_16x16x32_bf16 v[4:7], v[158:161], v[232:235], v[4:7]
	s_setprio 0
	s_setprio 1
	v_mfma_f32_16x16x32_bf16 v[56:59], v[154:157], v[190:193], v[56:59]
	v_mfma_f32_16x16x32_bf16 v[52:55], v[162:165], v[190:193], v[52:55]
	v_mfma_f32_16x16x32_bf16 v[40:43], v[154:157], v[216:219], v[40:43]
	v_mfma_f32_16x16x32_bf16 v[36:39], v[162:165], v[216:219], v[36:39]
	v_mfma_f32_16x16x32_bf16 v[24:27], v[154:157], v[228:231], v[24:27]
	v_mfma_f32_16x16x32_bf16 v[20:23], v[162:165], v[228:231], v[20:23]
	v_mfma_f32_16x16x32_bf16 v[8:11], v[154:157], v[236:239], v[8:11]
	v_mfma_f32_16x16x32_bf16 v[4:7], v[162:165], v[236:239], v[4:7]
	s_setprio 0
	s_setprio 1
	v_mfma_f32_16x16x32_bf16 v[60:63], v[166:169], v[182:185], v[60:63]
	v_mfma_f32_16x16x32_bf16 v[64:67], v[174:177], v[182:185], v[64:67]
	v_mfma_f32_16x16x32_bf16 v[44:47], v[166:169], v[212:215], v[44:47]
	v_mfma_f32_16x16x32_bf16 v[48:51], v[174:177], v[212:215], v[48:51]
	v_mfma_f32_16x16x32_bf16 v[28:31], v[166:169], v[224:227], v[28:31]
	v_mfma_f32_16x16x32_bf16 v[32:35], v[174:177], v[224:227], v[32:35]
	v_mfma_f32_16x16x32_bf16 v[12:15], v[166:169], v[232:235], v[12:15]
	v_mfma_f32_16x16x32_bf16 v[16:19], v[174:177], v[232:235], v[16:19]
	s_setprio 0
	s_setprio 1
	v_mfma_f32_16x16x32_bf16 v[60:63], v[170:173], v[190:193], v[60:63]
	v_mfma_f32_16x16x32_bf16 v[64:67], v[178:181], v[190:193], v[64:67]
	v_mfma_f32_16x16x32_bf16 v[44:47], v[170:173], v[216:219], v[44:47]
	v_mfma_f32_16x16x32_bf16 v[48:51], v[178:181], v[216:219], v[48:51]
	v_mfma_f32_16x16x32_bf16 v[28:31], v[170:173], v[228:231], v[28:31]
	v_mfma_f32_16x16x32_bf16 v[32:35], v[178:181], v[228:231], v[32:35]
	v_mfma_f32_16x16x32_bf16 v[12:15], v[170:173], v[236:239], v[12:15]
	v_mfma_f32_16x16x32_bf16 v[16:19], v[178:181], v[236:239], v[16:19]
	s_setprio 0
	s_barrier
	v_add_u32_e32 v2, s3, v152
	ds_read_b128 v[132:135], v2
	ds_read_b128 v[154:157], v2 offset:1024
	ds_read_b128 v[158:161], v2 offset:2048
	ds_read_b128 v[162:165], v2 offset:3072
	v_add_u32_e32 v2, s2, v152
	ds_read_b128 v[166:169], v2
	ds_read_b128 v[170:173], v2 offset:1024
	ds_read_b128 v[174:177], v2 offset:2048
	ds_read_b128 v[178:181], v2 offset:3072
	s_mov_b32 m0, s20
	v_lshl_add_u64 v[242:243], s[56:57], 0, v[144:145]
	ds_read_b128 v[182:185], v153 offset:32768
	ds_read_b128 v[190:193], v153 offset:33792
	ds_read_b128 v[212:215], v153 offset:34816
	ds_read_b128 v[216:219], v153 offset:35840
	ds_read_b128 v[224:227], v153 offset:36864
	ds_read_b128 v[228:231], v153 offset:37888
	ds_read_b128 v[232:235], v153 offset:38912
	ds_read_b128 v[236:239], v153 offset:39936
	global_load_lds_dwordx4 v[242:243], off
	v_lshl_add_u64 v[242:243], s[56:57], 0, v[146:147]
	s_mov_b32 m0, s21
	s_nop 0
	global_load_lds_dwordx4 v[242:243], off
	s_waitcnt vmcnt(8)
	s_waitcnt lgkmcnt(0)
	s_barrier
	s_setprio 1
	s_waitcnt lgkmcnt(0)
	v_mfma_f32_16x16x32_bf16 v[128:131], v[132:135], v[182:185], v[128:131]
	v_mfma_f32_16x16x32_bf16 v[124:127], v[158:161], v[182:185], v[124:127]
	v_mfma_f32_16x16x32_bf16 v[112:115], v[132:135], v[212:215], v[112:115]
	v_mfma_f32_16x16x32_bf16 v[108:111], v[158:161], v[212:215], v[108:111]
	v_mfma_f32_16x16x32_bf16 v[96:99], v[132:135], v[224:227], v[96:99]
	v_mfma_f32_16x16x32_bf16 v[92:95], v[158:161], v[224:227], v[92:95]
	v_mfma_f32_16x16x32_bf16 v[80:83], v[132:135], v[232:235], v[80:83]
	v_mfma_f32_16x16x32_bf16 v[76:79], v[158:161], v[232:235], v[76:79]
	s_setprio 0
	s_setprio 1
	v_mfma_f32_16x16x32_bf16 v[128:131], v[154:157], v[190:193], v[128:131]
	v_mfma_f32_16x16x32_bf16 v[124:127], v[162:165], v[190:193], v[124:127]
	v_mfma_f32_16x16x32_bf16 v[112:115], v[154:157], v[216:219], v[112:115]
	v_mfma_f32_16x16x32_bf16 v[108:111], v[162:165], v[216:219], v[108:111]
	v_mfma_f32_16x16x32_bf16 v[96:99], v[154:157], v[228:231], v[96:99]
	v_mfma_f32_16x16x32_bf16 v[92:95], v[162:165], v[228:231], v[92:95]
	v_mfma_f32_16x16x32_bf16 v[80:83], v[154:157], v[236:239], v[80:83]
	v_mfma_f32_16x16x32_bf16 v[76:79], v[162:165], v[236:239], v[76:79]
	s_setprio 0
	s_setprio 1
	v_mfma_f32_16x16x32_bf16 v[120:123], v[166:169], v[182:185], v[120:123]
	v_mfma_f32_16x16x32_bf16 v[116:119], v[174:177], v[182:185], v[116:119]
	v_mfma_f32_16x16x32_bf16 v[104:107], v[166:169], v[212:215], v[104:107]
	v_mfma_f32_16x16x32_bf16 v[100:103], v[174:177], v[212:215], v[100:103]
	v_mfma_f32_16x16x32_bf16 v[88:91], v[166:169], v[224:227], v[88:91]
	v_mfma_f32_16x16x32_bf16 v[84:87], v[174:177], v[224:227], v[84:87]
	v_mfma_f32_16x16x32_bf16 v[72:75], v[166:169], v[232:235], v[72:75]
	v_mfma_f32_16x16x32_bf16 v[68:71], v[174:177], v[232:235], v[68:71]
	s_setprio 0
	s_setprio 1
	v_mfma_f32_16x16x32_bf16 v[120:123], v[170:173], v[190:193], v[120:123]
	v_mfma_f32_16x16x32_bf16 v[116:119], v[178:181], v[190:193], v[116:119]
	v_mfma_f32_16x16x32_bf16 v[104:107], v[170:173], v[216:219], v[104:107]
	v_mfma_f32_16x16x32_bf16 v[100:103], v[178:181], v[216:219], v[100:103]
	v_mfma_f32_16x16x32_bf16 v[88:91], v[170:173], v[228:231], v[88:91]
	v_mfma_f32_16x16x32_bf16 v[84:87], v[178:181], v[228:231], v[84:87]
	v_mfma_f32_16x16x32_bf16 v[72:75], v[170:173], v[236:239], v[72:75]
	v_mfma_f32_16x16x32_bf16 v[68:71], v[178:181], v[236:239], v[68:71]
	s_setprio 0
	s_barrier
	s_mov_b32 m0, s64
	v_lshl_add_u64 v[148:149], v[148:149], 0, s[30:31]
	ds_read_b128 v[182:185], v153 offset:49152
	ds_read_b128 v[190:193], v153 offset:50176
	ds_read_b128 v[212:215], v153 offset:51200
	ds_read_b128 v[216:219], v153 offset:52224
	ds_read_b128 v[224:227], v153 offset:53248
	ds_read_b128 v[228:231], v153 offset:54272
	ds_read_b128 v[232:235], v153 offset:55296
	ds_read_b128 v[236:239], v153 offset:56320
	global_load_lds_dwordx4 v[148:149], off
	v_lshl_add_u64 v[148:149], v[186:187], 0, s[30:31]
	s_mov_b32 m0, s7
	s_nop 0
	global_load_lds_dwordx4 v[148:149], off
	v_lshl_add_u64 v[148:149], s[54:55], 0, v[136:137]
	s_mov_b32 m0, s70
	s_nop 0
	global_load_lds_dwordx4 v[148:149], off
	v_lshl_add_u64 v[148:149], s[54:55], 0, v[138:139]
	s_mov_b32 m0, s69
	s_nop 0
	global_load_lds_dwordx4 v[148:149], off
	v_lshl_add_u64 v[148:149], v[194:195], 0, s[30:31]
	s_mov_b32 m0, s24
	s_nop 0
	global_load_lds_dwordx4 v[148:149], off
	v_lshl_add_u64 v[148:149], v[240:241], 0, s[30:31]
	s_mov_b32 m0, s25
	s_nop 0
	global_load_lds_dwordx4 v[148:149], off
	s_waitcnt vmcnt(8)
	s_waitcnt lgkmcnt(0)
	s_barrier
	s_setprio 1
	s_waitcnt lgkmcnt(0)
	v_mfma_f32_16x16x32_bf16 v[56:59], v[132:135], v[182:185], v[56:59]
	v_mfma_f32_16x16x32_bf16 v[52:55], v[158:161], v[182:185], v[52:55]
	v_mfma_f32_16x16x32_bf16 v[40:43], v[132:135], v[212:215], v[40:43]
	v_mfma_f32_16x16x32_bf16 v[36:39], v[158:161], v[212:215], v[36:39]
	v_mfma_f32_16x16x32_bf16 v[24:27], v[132:135], v[224:227], v[24:27]
	v_mfma_f32_16x16x32_bf16 v[20:23], v[158:161], v[224:227], v[20:23]
	v_mfma_f32_16x16x32_bf16 v[8:11], v[132:135], v[232:235], v[8:11]
	v_mfma_f32_16x16x32_bf16 v[4:7], v[158:161], v[232:235], v[4:7]
	s_setprio 0
	s_setprio 1
	v_mfma_f32_16x16x32_bf16 v[56:59], v[154:157], v[190:193], v[56:59]
	v_mfma_f32_16x16x32_bf16 v[52:55], v[162:165], v[190:193], v[52:55]
	v_mfma_f32_16x16x32_bf16 v[40:43], v[154:157], v[216:219], v[40:43]
	v_mfma_f32_16x16x32_bf16 v[36:39], v[162:165], v[216:219], v[36:39]
	v_mfma_f32_16x16x32_bf16 v[24:27], v[154:157], v[228:231], v[24:27]
	v_mfma_f32_16x16x32_bf16 v[20:23], v[162:165], v[228:231], v[20:23]
	v_mfma_f32_16x16x32_bf16 v[8:11], v[154:157], v[236:239], v[8:11]
	v_mfma_f32_16x16x32_bf16 v[4:7], v[162:165], v[236:239], v[4:7]
	s_setprio 0
	s_setprio 1
	v_mfma_f32_16x16x32_bf16 v[60:63], v[166:169], v[182:185], v[60:63]
	v_mfma_f32_16x16x32_bf16 v[64:67], v[174:177], v[182:185], v[64:67]
	v_mfma_f32_16x16x32_bf16 v[44:47], v[166:169], v[212:215], v[44:47]
	v_mfma_f32_16x16x32_bf16 v[48:51], v[174:177], v[212:215], v[48:51]
	v_mfma_f32_16x16x32_bf16 v[28:31], v[166:169], v[224:227], v[28:31]
	v_mfma_f32_16x16x32_bf16 v[32:35], v[174:177], v[224:227], v[32:35]
	v_mfma_f32_16x16x32_bf16 v[12:15], v[166:169], v[232:235], v[12:15]
	v_mfma_f32_16x16x32_bf16 v[16:19], v[174:177], v[232:235], v[16:19]
	s_setprio 0
	s_setprio 1
	v_mfma_f32_16x16x32_bf16 v[60:63], v[170:173], v[190:193], v[60:63]
	v_mfma_f32_16x16x32_bf16 v[64:67], v[178:181], v[190:193], v[64:67]
	v_mfma_f32_16x16x32_bf16 v[44:47], v[170:173], v[216:219], v[44:47]
	v_mfma_f32_16x16x32_bf16 v[48:51], v[178:181], v[216:219], v[48:51]
	v_mfma_f32_16x16x32_bf16 v[28:31], v[170:173], v[228:231], v[28:31]
	v_mfma_f32_16x16x32_bf16 v[32:35], v[178:181], v[228:231], v[32:35]
	v_mfma_f32_16x16x32_bf16 v[12:15], v[170:173], v[236:239], v[12:15]
	v_mfma_f32_16x16x32_bf16 v[16:19], v[178:181], v[236:239], v[16:19]
	s_setprio 0
	s_barrier
	s_movk_i32 s7, 0x100
	s_andn2_b64 vcc, exec, s[52:53]
	s_mov_b64 s[54:55], -1
	s_mov_b64 s[52:53], 0
	s_cbranch_vccz .LBB0_1105
	s_and_b64 vcc, exec, s[36:37]
	s_cbranch_vccz .LBB0_1108
	s_barrier

.LBB0_1295:
	s_add_u32 s2, s46, 0x80
	s_addc_u32 s3, s47, 0
	s_cmp_eq_u32 s53, 4
	s_cselect_b32 s51, s25, s3
	s_cselect_b32 s50, s26, s2
	s_cselect_b32 s49, s27, s52
	s_cselect_b32 s48, s28, s29
	s_add_i32 s2, 0, 0x10000
	v_add_u32_e32 v155, s2, v148
	s_add_i32 s54, 0, 0x14000
	ds_read_b128 v[150:153], v155
	ds_read_b128 v[156:159], v155 offset:1024
	ds_read_b128 v[160:163], v155 offset:2048
	ds_read_b128 v[164:167], v155 offset:3072
	v_add_u32_e32 v155, s54, v148
	ds_read_b128 v[168:171], v155
	ds_read_b128 v[172:175], v155 offset:1024
	ds_read_b128 v[176:179], v155 offset:2048
	ds_read_b128 v[180:183], v155 offset:3072
	v_lshl_add_u64 v[194:195], s[46:47], 0, v[144:145]
	s_add_i32 m0, s15, 0xc000
	ds_read_b128 v[184:187], v149
	ds_read_b128 v[190:193], v149 offset:1024
	ds_read_b128 v[212:215], v149 offset:2048
	ds_read_b128 v[216:219], v149 offset:3072
	ds_read_b128 v[224:227], v149 offset:4096
	ds_read_b128 v[228:231], v149 offset:5120
	ds_read_b128 v[232:235], v149 offset:6144
	ds_read_b128 v[236:239], v149 offset:7168
	global_load_lds_dwordx4 v[194:195], off
	v_lshl_add_u64 v[194:195], s[46:47], 0, v[142:143]
	s_add_i32 m0, s15, 0xe000
	s_nop 0
	global_load_lds_dwordx4 v[194:195], off
	s_waitcnt vmcnt(8)
	s_waitcnt lgkmcnt(0)
	s_barrier
	s_setprio 1
	s_waitcnt lgkmcnt(0)
	v_mfma_f32_16x16x32_bf16 v[128:131], v[150:153], v[184:187], v[128:131]
	v_mfma_f32_16x16x32_bf16 v[124:127], v[160:163], v[184:187], v[124:127]
	v_mfma_f32_16x16x32_bf16 v[120:123], v[150:153], v[212:215], v[120:123]
	v_mfma_f32_16x16x32_bf16 v[116:119], v[160:163], v[212:215], v[116:119]
	v_mfma_f32_16x16x32_bf16 v[104:107], v[150:153], v[224:227], v[104:107]
	v_mfma_f32_16x16x32_bf16 v[100:103], v[160:163], v[224:227], v[100:103]
	v_mfma_f32_16x16x32_bf16 v[88:91], v[150:153], v[232:235], v[88:91]
	v_mfma_f32_16x16x32_bf16 v[84:87], v[160:163], v[232:235], v[84:87]
	s_setprio 0
	s_setprio 1
	v_mfma_f32_16x16x32_bf16 v[128:131], v[156:159], v[190:193], v[128:131]
	v_mfma_f32_16x16x32_bf16 v[124:127], v[164:167], v[190:193], v[124:127]
	v_mfma_f32_16x16x32_bf16 v[120:123], v[156:159], v[216:219], v[120:123]
	v_mfma_f32_16x16x32_bf16 v[116:119], v[164:167], v[216:219], v[116:119]
	v_mfma_f32_16x16x32_bf16 v[104:107], v[156:159], v[228:231], v[104:107]
	v_mfma_f32_16x16x32_bf16 v[100:103], v[164:167], v[228:231], v[100:103]
	v_mfma_f32_16x16x32_bf16 v[88:91], v[156:159], v[236:239], v[88:91]
	v_mfma_f32_16x16x32_bf16 v[84:87], v[164:167], v[236:239], v[84:87]
	s_setprio 0
	s_setprio 1
	v_mfma_f32_16x16x32_bf16 v[112:115], v[168:171], v[184:187], v[112:115]
	v_mfma_f32_16x16x32_bf16 v[108:111], v[176:179], v[184:187], v[108:111]
	v_mfma_f32_16x16x32_bf16 v[96:99], v[168:171], v[212:215], v[96:99]
	v_mfma_f32_16x16x32_bf16 v[92:95], v[176:179], v[212:215], v[92:95]
	v_mfma_f32_16x16x32_bf16 v[76:79], v[168:171], v[224:227], v[76:79]
	v_mfma_f32_16x16x32_bf16 v[68:71], v[176:179], v[224:227], v[68:71]
	v_mfma_f32_16x16x32_bf16 v[56:59], v[168:171], v[232:235], v[56:59]
	v_mfma_f32_16x16x32_bf16 v[44:47], v[176:179], v[232:235], v[44:47]
	s_setprio 0
	s_setprio 1
	v_mfma_f32_16x16x32_bf16 v[112:115], v[172:175], v[190:193], v[112:115]
	v_mfma_f32_16x16x32_bf16 v[108:111], v[180:183], v[190:193], v[108:111]
	v_mfma_f32_16x16x32_bf16 v[96:99], v[172:175], v[216:219], v[96:99]
	v_mfma_f32_16x16x32_bf16 v[92:95], v[180:183], v[216:219], v[92:95]
	v_mfma_f32_16x16x32_bf16 v[76:79], v[172:175], v[228:231], v[76:79]
	v_mfma_f32_16x16x32_bf16 v[68:71], v[180:183], v[228:231], v[68:71]
	v_mfma_f32_16x16x32_bf16 v[56:59], v[172:175], v[236:239], v[56:59]
	v_mfma_f32_16x16x32_bf16 v[44:47], v[180:183], v[236:239], v[44:47]
	s_setprio 0
	s_barrier
	s_add_i32 s2, s2, s12
	v_lshl_add_u64 v[194:195], s[48:49], 0, v[2:3]
	s_mov_b32 m0, s2
	ds_read_b128 v[184:187], v149 offset:16384
	ds_read_b128 v[190:193], v149 offset:17408
	ds_read_b128 v[212:215], v149 offset:18432
	ds_read_b128 v[216:219], v149 offset:19456
	ds_read_b128 v[224:227], v149 offset:20480
	ds_read_b128 v[228:231], v149 offset:21504
	ds_read_b128 v[232:235], v149 offset:22528
	ds_read_b128 v[236:239], v149 offset:23552
	global_load_lds_dwordx4 v[194:195], off
	s_add_i32 m0, s2, 0x2000
	s_add_u32 s2, s48, 0x20000
	v_lshl_add_u64 v[240:241], s[48:49], 0, v[132:133]
	s_addc_u32 s3, s49, 0
	s_add_i32 s54, s54, s12
	global_load_lds_dwordx4 v[240:241], off
	v_lshl_add_u64 v[242:243], s[2:3], 0, v[2:3]
	s_mov_b32 m0, s54
	v_lshl_add_u64 v[244:245], s[50:51], 0, v[136:137]
	global_load_lds_dwordx4 v[242:243], off
	v_lshl_add_u64 v[242:243], s[2:3], 0, v[132:133]
	s_add_i32 m0, s54, 0x2000
	s_nop 0
	global_load_lds_dwordx4 v[242:243], off
	v_lshl_add_u64 v[242:243], s[50:51], 0, v[134:135]
	s_mov_b32 m0, s15
	s_nop 0
	global_load_lds_dwordx4 v[242:243], off
	s_mov_b32 m0, s16
	s_nop 0
	global_load_lds_dwordx4 v[244:245], off
	s_waitcnt vmcnt(8)
	s_waitcnt lgkmcnt(0)
	s_barrier
	s_setprio 1
	s_waitcnt lgkmcnt(0)
	v_mfma_f32_16x16x32_bf16 v[36:39], v[150:153], v[184:187], v[36:39]
	v_mfma_f32_16x16x32_bf16 v[28:31], v[160:163], v[184:187], v[28:31]
	v_mfma_f32_16x16x32_bf16 v[24:27], v[150:153], v[212:215], v[24:27]
	v_mfma_f32_16x16x32_bf16 v[20:23], v[160:163], v[212:215], v[20:23]
	v_mfma_f32_16x16x32_bf16 v[16:19], v[150:153], v[224:227], v[16:19]
	v_mfma_f32_16x16x32_bf16 v[12:15], v[160:163], v[224:227], v[12:15]
	v_mfma_f32_16x16x32_bf16 v[8:11], v[150:153], v[232:235], v[8:11]
	v_mfma_f32_16x16x32_bf16 v[4:7], v[160:163], v[232:235], v[4:7]
	s_setprio 0
	s_setprio 1
	v_mfma_f32_16x16x32_bf16 v[36:39], v[156:159], v[190:193], v[36:39]
	v_mfma_f32_16x16x32_bf16 v[28:31], v[164:167], v[190:193], v[28:31]
	v_mfma_f32_16x16x32_bf16 v[24:27], v[156:159], v[216:219], v[24:27]
	v_mfma_f32_16x16x32_bf16 v[20:23], v[164:167], v[216:219], v[20:23]
	v_mfma_f32_16x16x32_bf16 v[16:19], v[156:159], v[228:231], v[16:19]
	v_mfma_f32_16x16x32_bf16 v[12:15], v[164:167], v[228:231], v[12:15]
	v_mfma_f32_16x16x32_bf16 v[8:11], v[156:159], v[236:239], v[8:11]
	v_mfma_f32_16x16x32_bf16 v[4:7], v[164:167], v[236:239], v[4:7]
	s_setprio 0
	s_setprio 1
	v_mfma_f32_16x16x32_bf16 v[72:75], v[168:171], v[184:187], v[72:75]
	v_mfma_f32_16x16x32_bf16 v[80:83], v[176:179], v[184:187], v[80:83]
	v_mfma_f32_16x16x32_bf16 v[60:63], v[168:171], v[212:215], v[60:63]
	v_mfma_f32_16x16x32_bf16 v[64:67], v[176:179], v[212:215], v[64:67]
	v_mfma_f32_16x16x32_bf16 v[48:51], v[168:171], v[224:227], v[48:51]
	v_mfma_f32_16x16x32_bf16 v[52:55], v[176:179], v[224:227], v[52:55]
	v_mfma_f32_16x16x32_bf16 v[32:35], v[168:171], v[232:235], v[32:35]
	v_mfma_f32_16x16x32_bf16 v[40:43], v[176:179], v[232:235], v[40:43]
	s_setprio 0
	s_setprio 1
	v_mfma_f32_16x16x32_bf16 v[72:75], v[172:175], v[190:193], v[72:75]
	v_mfma_f32_16x16x32_bf16 v[80:83], v[180:183], v[190:193], v[80:83]
	v_mfma_f32_16x16x32_bf16 v[60:63], v[172:175], v[216:219], v[60:63]
	v_mfma_f32_16x16x32_bf16 v[64:67], v[180:183], v[216:219], v[64:67]
	v_mfma_f32_16x16x32_bf16 v[48:51], v[172:175], v[228:231], v[48:51]
	v_mfma_f32_16x16x32_bf16 v[52:55], v[180:183], v[228:231], v[52:55]
	v_mfma_f32_16x16x32_bf16 v[32:35], v[172:175], v[236:239], v[32:35]
	v_mfma_f32_16x16x32_bf16 v[40:43], v[180:183], v[236:239], v[40:43]
	s_setprio 0
	s_barrier
	s_add_i32 s2, 0, 0x18000
	v_add_u32_e32 v155, s2, v148
	s_add_i32 s54, 0, 0x1c000
	ds_read_b128 v[150:153], v155
	ds_read_b128 v[156:159], v155 offset:1024
	ds_read_b128 v[160:163], v155 offset:2048
	ds_read_b128 v[164:167], v155 offset:3072
	v_add_u32_e32 v155, s54, v148
	ds_read_b128 v[168:171], v155
	ds_read_b128 v[172:175], v155 offset:1024
	ds_read_b128 v[176:179], v155 offset:2048
	ds_read_b128 v[180:183], v155 offset:3072
	s_mov_b32 m0, s17
	v_lshl_add_u64 v[246:247], s[50:51], 0, v[138:139]
	ds_read_b128 v[184:187], v149 offset:32768
	ds_read_b128 v[190:193], v149 offset:33792
	ds_read_b128 v[212:215], v149 offset:34816
	ds_read_b128 v[216:219], v149 offset:35840
	ds_read_b128 v[224:227], v149 offset:36864
	ds_read_b128 v[228:231], v149 offset:37888
	ds_read_b128 v[232:235], v149 offset:38912
	ds_read_b128 v[236:239], v149 offset:39936
	global_load_lds_dwordx4 v[246:247], off
	v_lshl_add_u64 v[246:247], s[50:51], 0, v[140:141]
	s_mov_b32 m0, s18
	s_nop 0
	global_load_lds_dwordx4 v[246:247], off
	s_waitcnt vmcnt(8)
	s_waitcnt lgkmcnt(0)
	s_barrier
	s_setprio 1
	s_waitcnt lgkmcnt(0)
	v_mfma_f32_16x16x32_bf16 v[128:131], v[150:153], v[184:187], v[128:131]
	v_mfma_f32_16x16x32_bf16 v[124:127], v[160:163], v[184:187], v[124:127]
	v_mfma_f32_16x16x32_bf16 v[120:123], v[150:153], v[212:215], v[120:123]
	v_mfma_f32_16x16x32_bf16 v[116:119], v[160:163], v[212:215], v[116:119]
	v_mfma_f32_16x16x32_bf16 v[104:107], v[150:153], v[224:227], v[104:107]
	v_mfma_f32_16x16x32_bf16 v[100:103], v[160:163], v[224:227], v[100:103]
	v_mfma_f32_16x16x32_bf16 v[88:91], v[150:153], v[232:235], v[88:91]
	v_mfma_f32_16x16x32_bf16 v[84:87], v[160:163], v[232:235], v[84:87]
	s_setprio 0
	s_setprio 1
	v_mfma_f32_16x16x32_bf16 v[128:131], v[156:159], v[190:193], v[128:131]
	v_mfma_f32_16x16x32_bf16 v[124:127], v[164:167], v[190:193], v[124:127]
	v_mfma_f32_16x16x32_bf16 v[120:123], v[156:159], v[216:219], v[120:123]
	v_mfma_f32_16x16x32_bf16 v[116:119], v[164:167], v[216:219], v[116:119]
	v_mfma_f32_16x16x32_bf16 v[104:107], v[156:159], v[228:231], v[104:107]
	v_mfma_f32_16x16x32_bf16 v[100:103], v[164:167], v[228:231], v[100:103]
	v_mfma_f32_16x16x32_bf16 v[88:91], v[156:159], v[236:239], v[88:91]
	v_mfma_f32_16x16x32_bf16 v[84:87], v[164:167], v[236:239], v[84:87]
	s_setprio 0
	s_setprio 1
	v_mfma_f32_16x16x32_bf16 v[112:115], v[168:171], v[184:187], v[112:115]
	v_mfma_f32_16x16x32_bf16 v[108:111], v[176:179], v[184:187], v[108:111]
	v_mfma_f32_16x16x32_bf16 v[96:99], v[168:171], v[212:215], v[96:99]
	v_mfma_f32_16x16x32_bf16 v[92:95], v[176:179], v[212:215], v[92:95]
	v_mfma_f32_16x16x32_bf16 v[76:79], v[168:171], v[224:227], v[76:79]
	v_mfma_f32_16x16x32_bf16 v[68:71], v[176:179], v[224:227], v[68:71]
	v_mfma_f32_16x16x32_bf16 v[56:59], v[168:171], v[232:235], v[56:59]
	v_mfma_f32_16x16x32_bf16 v[44:47], v[176:179], v[232:235], v[44:47]
	s_setprio 0
	s_setprio 1
	v_mfma_f32_16x16x32_bf16 v[112:115], v[172:175], v[190:193], v[112:115]
	v_mfma_f32_16x16x32_bf16 v[108:111], v[180:183], v[190:193], v[108:111]
	v_mfma_f32_16x16x32_bf16 v[96:99], v[172:175], v[216:219], v[96:99]
	v_mfma_f32_16x16x32_bf16 v[92:95], v[180:183], v[216:219], v[92:95]
	v_mfma_f32_16x16x32_bf16 v[76:79], v[172:175], v[228:231], v[76:79]
	v_mfma_f32_16x16x32_bf16 v[68:71], v[180:183], v[228:231], v[68:71]
	v_mfma_f32_16x16x32_bf16 v[56:59], v[172:175], v[236:239], v[56:59]
	v_mfma_f32_16x16x32_bf16 v[44:47], v[180:183], v[236:239], v[44:47]
	s_setprio 0
	s_barrier
	s_add_i32 s2, s2, s12
	v_lshl_add_u64 v[194:195], v[194:195], 0, s[30:31]
	s_mov_b32 m0, s2
	ds_read_b128 v[184:187], v149 offset:49152
	ds_read_b128 v[190:193], v149 offset:50176
	ds_read_b128 v[212:215], v149 offset:51200
	ds_read_b128 v[216:219], v149 offset:52224
	ds_read_b128 v[224:227], v149 offset:53248
	ds_read_b128 v[228:231], v149 offset:54272
	ds_read_b128 v[232:235], v149 offset:55296
	ds_read_b128 v[236:239], v149 offset:56320
	global_load_lds_dwordx4 v[194:195], off
	s_add_i32 m0, s2, 0x2000
	s_add_u32 s2, s48, 0x20080
	v_lshl_add_u64 v[194:195], v[240:241], 0, s[30:31]
	s_addc_u32 s3, s49, 0
	s_add_i32 s48, s54, s12
	global_load_lds_dwordx4 v[194:195], off
	v_lshl_add_u64 v[194:195], s[2:3], 0, v[2:3]
	s_mov_b32 m0, s48
	s_nop 0
	global_load_lds_dwordx4 v[194:195], off
	v_lshl_add_u64 v[194:195], s[2:3], 0, v[132:133]
	s_add_i32 m0, s48, 0x2000
	s_nop 0
	global_load_lds_dwordx4 v[194:195], off
	v_lshl_add_u64 v[194:195], v[242:243], 0, s[30:31]
	s_mov_b32 m0, s19
	s_nop 0
	global_load_lds_dwordx4 v[194:195], off
	v_lshl_add_u64 v[194:195], v[244:245], 0, s[30:31]
	s_mov_b32 m0, s20
	s_nop 0
	global_load_lds_dwordx4 v[194:195], off
	s_waitcnt vmcnt(8)
	s_waitcnt lgkmcnt(0)
	s_barrier
	s_setprio 1
	s_waitcnt lgkmcnt(0)
	v_mfma_f32_16x16x32_bf16 v[36:39], v[150:153], v[184:187], v[36:39]
	v_mfma_f32_16x16x32_bf16 v[28:31], v[160:163], v[184:187], v[28:31]
	v_mfma_f32_16x16x32_bf16 v[24:27], v[150:153], v[212:215], v[24:27]
	v_mfma_f32_16x16x32_bf16 v[20:23], v[160:163], v[212:215], v[20:23]
	v_mfma_f32_16x16x32_bf16 v[16:19], v[150:153], v[224:227], v[16:19]
	v_mfma_f32_16x16x32_bf16 v[12:15], v[160:163], v[224:227], v[12:15]
	v_mfma_f32_16x16x32_bf16 v[8:11], v[150:153], v[232:235], v[8:11]
	v_mfma_f32_16x16x32_bf16 v[4:7], v[160:163], v[232:235], v[4:7]
	s_setprio 0
	s_setprio 1
	v_mfma_f32_16x16x32_bf16 v[36:39], v[156:159], v[190:193], v[36:39]
	v_mfma_f32_16x16x32_bf16 v[28:31], v[164:167], v[190:193], v[28:31]
	v_mfma_f32_16x16x32_bf16 v[24:27], v[156:159], v[216:219], v[24:27]
	v_mfma_f32_16x16x32_bf16 v[20:23], v[164:167], v[216:219], v[20:23]
	v_mfma_f32_16x16x32_bf16 v[16:19], v[156:159], v[228:231], v[16:19]
	v_mfma_f32_16x16x32_bf16 v[12:15], v[164:167], v[228:231], v[12:15]
	v_mfma_f32_16x16x32_bf16 v[8:11], v[156:159], v[236:239], v[8:11]
	v_mfma_f32_16x16x32_bf16 v[4:7], v[164:167], v[236:239], v[4:7]
	s_setprio 0
	s_setprio 1
	v_mfma_f32_16x16x32_bf16 v[72:75], v[168:171], v[184:187], v[72:75]
	v_mfma_f32_16x16x32_bf16 v[80:83], v[176:179], v[184:187], v[80:83]
	v_mfma_f32_16x16x32_bf16 v[60:63], v[168:171], v[212:215], v[60:63]
	v_mfma_f32_16x16x32_bf16 v[64:67], v[176:179], v[212:215], v[64:67]
	v_mfma_f32_16x16x32_bf16 v[48:51], v[168:171], v[224:227], v[48:51]
	v_mfma_f32_16x16x32_bf16 v[52:55], v[176:179], v[224:227], v[52:55]
	v_mfma_f32_16x16x32_bf16 v[32:35], v[168:171], v[232:235], v[32:35]
	v_mfma_f32_16x16x32_bf16 v[40:43], v[176:179], v[232:235], v[40:43]
	s_setprio 0
	s_setprio 1
	v_mfma_f32_16x16x32_bf16 v[72:75], v[172:175], v[190:193], v[72:75]
	v_mfma_f32_16x16x32_bf16 v[80:83], v[180:183], v[190:193], v[80:83]
	v_mfma_f32_16x16x32_bf16 v[60:63], v[172:175], v[216:219], v[60:63]
	v_mfma_f32_16x16x32_bf16 v[64:67], v[180:183], v[216:219], v[64:67]
	v_mfma_f32_16x16x32_bf16 v[48:51], v[172:175], v[228:231], v[48:51]
	v_mfma_f32_16x16x32_bf16 v[52:55], v[180:183], v[228:231], v[52:55]
	v_mfma_f32_16x16x32_bf16 v[32:35], v[172:175], v[236:239], v[32:35]
	v_mfma_f32_16x16x32_bf16 v[40:43], v[180:183], v[236:239], v[40:43]
	s_setprio 0
	s_barrier
	s_add_i32 s53, s53, 2
	s_add_u32 s46, s46, 0x100
	s_addc_u32 s47, s47, 0
	s_add_u32 s29, s29, 0x100
	s_addc_u32 s52, s52, 0
	s_cmp_gt_u32 s53, 5
	s_cbranch_scc0 .LBB0_1295
	s_and_b64 vcc, exec, s[38:39]
	v_readlane_b32 s26, v254, 28
	v_readlane_b32 s27, v254, 29
	s_cbranch_vccz .LBB0_1298
	s_barrier

.LBB0_1319:
	s_add_u32 s2, s46, 0x80
	s_addc_u32 s3, s47, 0
	s_cmp_eq_u32 s58, 60
	s_cselect_b32 s51, s52, s3
	s_cselect_b32 s50, s53, s2
	s_cselect_b32 s49, s54, s57
	s_cselect_b32 s48, s55, s56
	s_add_i32 s2, 0, 0x10000
	v_add_u32_e32 v2, s2, v157
	s_add_i32 s59, 0, 0x14000
	ds_read_b128 v[148:151], v2
	ds_read_b128 v[160:163], v2 offset:1024
	ds_read_b128 v[164:167], v2 offset:2048
	ds_read_b128 v[168:171], v2 offset:3072
	v_add_u32_e32 v2, s59, v157
	ds_read_b128 v[172:175], v2
	ds_read_b128 v[176:179], v2 offset:1024
	ds_read_b128 v[180:183], v2 offset:2048
	ds_read_b128 v[184:187], v2 offset:3072
	v_lshl_add_u64 v[152:153], s[46:47], 0, v[146:147]
	s_add_i32 m0, s17, 0xc000
	ds_read_b128 v[190:193], v158
	ds_read_b128 v[212:215], v158 offset:1024
	ds_read_b128 v[216:219], v158 offset:2048
	ds_read_b128 v[224:227], v158 offset:3072
	ds_read_b128 v[228:231], v158 offset:4096
	ds_read_b128 v[232:235], v158 offset:5120
	ds_read_b128 v[236:239], v158 offset:6144
	ds_read_b128 v[240:243], v158 offset:7168
	global_load_lds_dwordx4 v[152:153], off
	v_lshl_add_u64 v[152:153], s[46:47], 0, v[144:145]
	s_add_i32 m0, s17, 0xe000
	s_nop 0
	global_load_lds_dwordx4 v[152:153], off
	s_waitcnt vmcnt(8)
	s_waitcnt lgkmcnt(0)
	s_barrier
	s_setprio 1
	s_waitcnt lgkmcnt(0)
	v_mfma_f32_16x16x32_bf16 v[128:131], v[148:151], v[190:193], v[128:131]
	v_mfma_f32_16x16x32_bf16 v[124:127], v[164:167], v[190:193], v[124:127]
	v_mfma_f32_16x16x32_bf16 v[112:115], v[148:151], v[216:219], v[112:115]
	v_mfma_f32_16x16x32_bf16 v[108:111], v[164:167], v[216:219], v[108:111]
	v_mfma_f32_16x16x32_bf16 v[96:99], v[148:151], v[228:231], v[96:99]
	v_mfma_f32_16x16x32_bf16 v[92:95], v[164:167], v[228:231], v[92:95]
	v_mfma_f32_16x16x32_bf16 v[80:83], v[148:151], v[236:239], v[80:83]
	v_mfma_f32_16x16x32_bf16 v[76:79], v[164:167], v[236:239], v[76:79]
	s_setprio 0
	s_setprio 1
	v_mfma_f32_16x16x32_bf16 v[128:131], v[160:163], v[212:215], v[128:131]
	v_mfma_f32_16x16x32_bf16 v[124:127], v[168:171], v[212:215], v[124:127]
	v_mfma_f32_16x16x32_bf16 v[112:115], v[160:163], v[224:227], v[112:115]
	v_mfma_f32_16x16x32_bf16 v[108:111], v[168:171], v[224:227], v[108:111]
	v_mfma_f32_16x16x32_bf16 v[96:99], v[160:163], v[232:235], v[96:99]
	v_mfma_f32_16x16x32_bf16 v[92:95], v[168:171], v[232:235], v[92:95]
	v_mfma_f32_16x16x32_bf16 v[80:83], v[160:163], v[240:243], v[80:83]
	v_mfma_f32_16x16x32_bf16 v[76:79], v[168:171], v[240:243], v[76:79]
	s_setprio 0
	s_setprio 1
	v_mfma_f32_16x16x32_bf16 v[120:123], v[172:175], v[190:193], v[120:123]
	v_mfma_f32_16x16x32_bf16 v[116:119], v[180:183], v[190:193], v[116:119]
	v_mfma_f32_16x16x32_bf16 v[104:107], v[172:175], v[216:219], v[104:107]
	v_mfma_f32_16x16x32_bf16 v[100:103], v[180:183], v[216:219], v[100:103]
	v_mfma_f32_16x16x32_bf16 v[88:91], v[172:175], v[228:231], v[88:91]
	v_mfma_f32_16x16x32_bf16 v[84:87], v[180:183], v[228:231], v[84:87]
	v_mfma_f32_16x16x32_bf16 v[72:75], v[172:175], v[236:239], v[72:75]
	v_mfma_f32_16x16x32_bf16 v[68:71], v[180:183], v[236:239], v[68:71]
	s_setprio 0
	s_setprio 1
	v_mfma_f32_16x16x32_bf16 v[120:123], v[176:179], v[212:215], v[120:123]
	v_mfma_f32_16x16x32_bf16 v[116:119], v[184:187], v[212:215], v[116:119]
	v_mfma_f32_16x16x32_bf16 v[104:107], v[176:179], v[224:227], v[104:107]
	v_mfma_f32_16x16x32_bf16 v[100:103], v[184:187], v[224:227], v[100:103]
	v_mfma_f32_16x16x32_bf16 v[88:91], v[176:179], v[232:235], v[88:91]
	v_mfma_f32_16x16x32_bf16 v[84:87], v[184:187], v[232:235], v[84:87]
	v_mfma_f32_16x16x32_bf16 v[72:75], v[176:179], v[240:243], v[72:75]
	v_mfma_f32_16x16x32_bf16 v[68:71], v[184:187], v[240:243], v[68:71]
	s_setprio 0
	s_barrier
	s_add_i32 s2, s2, s16
	v_lshl_add_u64 v[152:153], s[48:49], 0, v[132:133]
	s_mov_b32 m0, s2
	ds_read_b128 v[190:193], v158 offset:16384
	ds_read_b128 v[212:215], v158 offset:17408
	ds_read_b128 v[216:219], v158 offset:18432
	ds_read_b128 v[224:227], v158 offset:19456
	ds_read_b128 v[228:231], v158 offset:20480
	ds_read_b128 v[232:235], v158 offset:21504
	ds_read_b128 v[236:239], v158 offset:22528
	ds_read_b128 v[240:243], v158 offset:23552
	global_load_lds_dwordx4 v[152:153], off
	s_add_i32 m0, s2, 0x2000
	s_add_u32 s2, s48, 0x100000
	v_lshl_add_u64 v[194:195], s[48:49], 0, v[134:135]
	s_addc_u32 s3, s49, 0
	s_add_i32 s59, s59, s16
	global_load_lds_dwordx4 v[194:195], off
	v_lshl_add_u64 v[244:245], s[2:3], 0, v[132:133]
	s_mov_b32 m0, s59
	v_lshl_add_u64 v[246:247], s[50:51], 0, v[138:139]
	global_load_lds_dwordx4 v[244:245], off
	v_lshl_add_u64 v[244:245], s[2:3], 0, v[134:135]
	s_add_i32 m0, s59, 0x2000
	s_nop 0
	global_load_lds_dwordx4 v[244:245], off
	v_lshl_add_u64 v[244:245], s[50:51], 0, v[136:137]
	s_mov_b32 m0, s17
	s_nop 0
	global_load_lds_dwordx4 v[244:245], off
	s_mov_b32 m0, s18
	s_nop 0
	global_load_lds_dwordx4 v[246:247], off
	s_waitcnt vmcnt(8)
	s_waitcnt lgkmcnt(0)
	s_barrier
	s_setprio 1
	s_waitcnt lgkmcnt(0)
	v_mfma_f32_16x16x32_bf16 v[56:59], v[148:151], v[190:193], v[56:59]
	v_mfma_f32_16x16x32_bf16 v[52:55], v[164:167], v[190:193], v[52:55]
	v_mfma_f32_16x16x32_bf16 v[40:43], v[148:151], v[216:219], v[40:43]
	v_mfma_f32_16x16x32_bf16 v[36:39], v[164:167], v[216:219], v[36:39]
	v_mfma_f32_16x16x32_bf16 v[24:27], v[148:151], v[228:231], v[24:27]
	v_mfma_f32_16x16x32_bf16 v[20:23], v[164:167], v[228:231], v[20:23]
	v_mfma_f32_16x16x32_bf16 v[8:11], v[148:151], v[236:239], v[8:11]
	v_mfma_f32_16x16x32_bf16 v[4:7], v[164:167], v[236:239], v[4:7]
	s_setprio 0
	s_setprio 1
	v_mfma_f32_16x16x32_bf16 v[56:59], v[160:163], v[212:215], v[56:59]
	v_mfma_f32_16x16x32_bf16 v[52:55], v[168:171], v[212:215], v[52:55]
	v_mfma_f32_16x16x32_bf16 v[40:43], v[160:163], v[224:227], v[40:43]
	v_mfma_f32_16x16x32_bf16 v[36:39], v[168:171], v[224:227], v[36:39]
	v_mfma_f32_16x16x32_bf16 v[24:27], v[160:163], v[232:235], v[24:27]
	v_mfma_f32_16x16x32_bf16 v[20:23], v[168:171], v[232:235], v[20:23]
	v_mfma_f32_16x16x32_bf16 v[8:11], v[160:163], v[240:243], v[8:11]
	v_mfma_f32_16x16x32_bf16 v[4:7], v[168:171], v[240:243], v[4:7]
	s_setprio 0
	s_setprio 1
	v_mfma_f32_16x16x32_bf16 v[60:63], v[172:175], v[190:193], v[60:63]
	v_mfma_f32_16x16x32_bf16 v[64:67], v[180:183], v[190:193], v[64:67]
	v_mfma_f32_16x16x32_bf16 v[44:47], v[172:175], v[216:219], v[44:47]
	v_mfma_f32_16x16x32_bf16 v[48:51], v[180:183], v[216:219], v[48:51]
	v_mfma_f32_16x16x32_bf16 v[28:31], v[172:175], v[228:231], v[28:31]
	v_mfma_f32_16x16x32_bf16 v[32:35], v[180:183], v[228:231], v[32:35]
	v_mfma_f32_16x16x32_bf16 v[12:15], v[172:175], v[236:239], v[12:15]
	v_mfma_f32_16x16x32_bf16 v[16:19], v[180:183], v[236:239], v[16:19]
	s_setprio 0
	s_setprio 1
	v_mfma_f32_16x16x32_bf16 v[60:63], v[176:179], v[212:215], v[60:63]
	v_mfma_f32_16x16x32_bf16 v[64:67], v[184:187], v[212:215], v[64:67]
	v_mfma_f32_16x16x32_bf16 v[44:47], v[176:179], v[224:227], v[44:47]
	v_mfma_f32_16x16x32_bf16 v[48:51], v[184:187], v[224:227], v[48:51]
	v_mfma_f32_16x16x32_bf16 v[28:31], v[176:179], v[232:235], v[28:31]
	v_mfma_f32_16x16x32_bf16 v[32:35], v[184:187], v[232:235], v[32:35]
	v_mfma_f32_16x16x32_bf16 v[12:15], v[176:179], v[240:243], v[12:15]
	v_mfma_f32_16x16x32_bf16 v[16:19], v[184:187], v[240:243], v[16:19]
	s_setprio 0
	s_barrier
	s_add_i32 s2, 0, 0x18000
	v_add_u32_e32 v2, s2, v157
	s_add_i32 s59, 0, 0x1c000
	ds_read_b128 v[148:151], v2
	ds_read_b128 v[160:163], v2 offset:1024
	ds_read_b128 v[164:167], v2 offset:2048
	ds_read_b128 v[168:171], v2 offset:3072
	v_add_u32_e32 v2, s59, v157
	ds_read_b128 v[172:175], v2
	ds_read_b128 v[176:179], v2 offset:1024
	ds_read_b128 v[180:183], v2 offset:2048
	ds_read_b128 v[184:187], v2 offset:3072
	s_mov_b32 m0, s19
	v_lshl_add_u64 v[248:249], s[50:51], 0, v[140:141]
	ds_read_b128 v[190:193], v158 offset:32768
	ds_read_b128 v[212:215], v158 offset:33792
	ds_read_b128 v[216:219], v158 offset:34816
	ds_read_b128 v[224:227], v158 offset:35840
	ds_read_b128 v[228:231], v158 offset:36864
	ds_read_b128 v[232:235], v158 offset:37888
	ds_read_b128 v[236:239], v158 offset:38912
	ds_read_b128 v[240:243], v158 offset:39936
	global_load_lds_dwordx4 v[248:249], off
	v_lshl_add_u64 v[248:249], s[50:51], 0, v[142:143]
	s_mov_b32 m0, s20
	s_nop 0
	global_load_lds_dwordx4 v[248:249], off
	s_waitcnt vmcnt(8)
	s_waitcnt lgkmcnt(0)
	s_barrier
	s_setprio 1
	s_waitcnt lgkmcnt(0)
	v_mfma_f32_16x16x32_bf16 v[128:131], v[148:151], v[190:193], v[128:131]
	v_mfma_f32_16x16x32_bf16 v[124:127], v[164:167], v[190:193], v[124:127]
	v_mfma_f32_16x16x32_bf16 v[112:115], v[148:151], v[216:219], v[112:115]
	v_mfma_f32_16x16x32_bf16 v[108:111], v[164:167], v[216:219], v[108:111]
	v_mfma_f32_16x16x32_bf16 v[96:99], v[148:151], v[228:231], v[96:99]
	v_mfma_f32_16x16x32_bf16 v[92:95], v[164:167], v[228:231], v[92:95]
	v_mfma_f32_16x16x32_bf16 v[80:83], v[148:151], v[236:239], v[80:83]
	v_mfma_f32_16x16x32_bf16 v[76:79], v[164:167], v[236:239], v[76:79]
	s_setprio 0
	s_setprio 1
	v_mfma_f32_16x16x32_bf16 v[128:131], v[160:163], v[212:215], v[128:131]
	v_mfma_f32_16x16x32_bf16 v[124:127], v[168:171], v[212:215], v[124:127]
	v_mfma_f32_16x16x32_bf16 v[112:115], v[160:163], v[224:227], v[112:115]
	v_mfma_f32_16x16x32_bf16 v[108:111], v[168:171], v[224:227], v[108:111]
	v_mfma_f32_16x16x32_bf16 v[96:99], v[160:163], v[232:235], v[96:99]
	v_mfma_f32_16x16x32_bf16 v[92:95], v[168:171], v[232:235], v[92:95]
	v_mfma_f32_16x16x32_bf16 v[80:83], v[160:163], v[240:243], v[80:83]
	v_mfma_f32_16x16x32_bf16 v[76:79], v[168:171], v[240:243], v[76:79]
	s_setprio 0
	s_setprio 1
	v_mfma_f32_16x16x32_bf16 v[120:123], v[172:175], v[190:193], v[120:123]
	v_mfma_f32_16x16x32_bf16 v[116:119], v[180:183], v[190:193], v[116:119]
	v_mfma_f32_16x16x32_bf16 v[104:107], v[172:175], v[216:219], v[104:107]
	v_mfma_f32_16x16x32_bf16 v[100:103], v[180:183], v[216:219], v[100:103]
	v_mfma_f32_16x16x32_bf16 v[88:91], v[172:175], v[228:231], v[88:91]
	v_mfma_f32_16x16x32_bf16 v[84:87], v[180:183], v[228:231], v[84:87]
	v_mfma_f32_16x16x32_bf16 v[72:75], v[172:175], v[236:239], v[72:75]
	v_mfma_f32_16x16x32_bf16 v[68:71], v[180:183], v[236:239], v[68:71]
	s_setprio 0
	s_setprio 1
	v_mfma_f32_16x16x32_bf16 v[120:123], v[176:179], v[212:215], v[120:123]
	v_mfma_f32_16x16x32_bf16 v[116:119], v[184:187], v[212:215], v[116:119]
	v_mfma_f32_16x16x32_bf16 v[104:107], v[176:179], v[224:227], v[104:107]
	v_mfma_f32_16x16x32_bf16 v[100:103], v[184:187], v[224:227], v[100:103]
	v_mfma_f32_16x16x32_bf16 v[88:91], v[176:179], v[232:235], v[88:91]
	v_mfma_f32_16x16x32_bf16 v[84:87], v[184:187], v[232:235], v[84:87]
	v_mfma_f32_16x16x32_bf16 v[72:75], v[176:179], v[240:243], v[72:75]
	v_mfma_f32_16x16x32_bf16 v[68:71], v[184:187], v[240:243], v[68:71]
	s_setprio 0
	s_barrier
	s_add_i32 s2, s2, s16
	v_lshl_add_u64 v[152:153], v[152:153], 0, s[30:31]
	s_mov_b32 m0, s2
	ds_read_b128 v[190:193], v158 offset:49152
	ds_read_b128 v[212:215], v158 offset:50176
	ds_read_b128 v[216:219], v158 offset:51200
	ds_read_b128 v[224:227], v158 offset:52224
	ds_read_b128 v[228:231], v158 offset:53248
	ds_read_b128 v[232:235], v158 offset:54272
	ds_read_b128 v[236:239], v158 offset:55296
	ds_read_b128 v[240:243], v158 offset:56320
	global_load_lds_dwordx4 v[152:153], off
	s_add_i32 m0, s2, 0x2000
	s_add_u32 s2, s48, 0x100080
	v_lshl_add_u64 v[152:153], v[194:195], 0, s[30:31]
	s_addc_u32 s3, s49, 0
	s_add_i32 s48, s59, s16
	global_load_lds_dwordx4 v[152:153], off
	v_lshl_add_u64 v[152:153], s[2:3], 0, v[132:133]
	s_mov_b32 m0, s48
	s_nop 0
	global_load_lds_dwordx4 v[152:153], off
	v_lshl_add_u64 v[152:153], s[2:3], 0, v[134:135]
	s_add_i32 m0, s48, 0x2000
	s_nop 0
	global_load_lds_dwordx4 v[152:153], off
	v_lshl_add_u64 v[152:153], v[244:245], 0, s[30:31]
	s_mov_b32 m0, s23
	s_nop 0
	global_load_lds_dwordx4 v[152:153], off
	v_lshl_add_u64 v[152:153], v[246:247], 0, s[30:31]
	s_mov_b32 m0, s24
	s_nop 0
	global_load_lds_dwordx4 v[152:153], off
	s_waitcnt vmcnt(8)
	s_waitcnt lgkmcnt(0)
	s_barrier
	s_setprio 1
	s_waitcnt lgkmcnt(0)
	v_mfma_f32_16x16x32_bf16 v[56:59], v[148:151], v[190:193], v[56:59]
	v_mfma_f32_16x16x32_bf16 v[52:55], v[164:167], v[190:193], v[52:55]
	v_mfma_f32_16x16x32_bf16 v[40:43], v[148:151], v[216:219], v[40:43]
	v_mfma_f32_16x16x32_bf16 v[36:39], v[164:167], v[216:219], v[36:39]
	v_mfma_f32_16x16x32_bf16 v[24:27], v[148:151], v[228:231], v[24:27]
	v_mfma_f32_16x16x32_bf16 v[20:23], v[164:167], v[228:231], v[20:23]
	v_mfma_f32_16x16x32_bf16 v[8:11], v[148:151], v[236:239], v[8:11]
	v_mfma_f32_16x16x32_bf16 v[4:7], v[164:167], v[236:239], v[4:7]
	s_setprio 0
	s_setprio 1
	v_mfma_f32_16x16x32_bf16 v[56:59], v[160:163], v[212:215], v[56:59]
	v_mfma_f32_16x16x32_bf16 v[52:55], v[168:171], v[212:215], v[52:55]
	v_mfma_f32_16x16x32_bf16 v[40:43], v[160:163], v[224:227], v[40:43]
	v_mfma_f32_16x16x32_bf16 v[36:39], v[168:171], v[224:227], v[36:39]
	v_mfma_f32_16x16x32_bf16 v[24:27], v[160:163], v[232:235], v[24:27]
	v_mfma_f32_16x16x32_bf16 v[20:23], v[168:171], v[232:235], v[20:23]
	v_mfma_f32_16x16x32_bf16 v[8:11], v[160:163], v[240:243], v[8:11]
	v_mfma_f32_16x16x32_bf16 v[4:7], v[168:171], v[240:243], v[4:7]
	s_setprio 0
	s_setprio 1
	v_mfma_f32_16x16x32_bf16 v[60:63], v[172:175], v[190:193], v[60:63]
	v_mfma_f32_16x16x32_bf16 v[64:67], v[180:183], v[190:193], v[64:67]
	v_mfma_f32_16x16x32_bf16 v[44:47], v[172:175], v[216:219], v[44:47]
	v_mfma_f32_16x16x32_bf16 v[48:51], v[180:183], v[216:219], v[48:51]
	v_mfma_f32_16x16x32_bf16 v[28:31], v[172:175], v[228:231], v[28:31]
	v_mfma_f32_16x16x32_bf16 v[32:35], v[180:183], v[228:231], v[32:35]
	v_mfma_f32_16x16x32_bf16 v[12:15], v[172:175], v[236:239], v[12:15]
	v_mfma_f32_16x16x32_bf16 v[16:19], v[180:183], v[236:239], v[16:19]
	s_setprio 0
	s_setprio 1
	v_mfma_f32_16x16x32_bf16 v[60:63], v[176:179], v[212:215], v[60:63]
	v_mfma_f32_16x16x32_bf16 v[64:67], v[184:187], v[212:215], v[64:67]
	v_mfma_f32_16x16x32_bf16 v[44:47], v[176:179], v[224:227], v[44:47]
	v_mfma_f32_16x16x32_bf16 v[48:51], v[184:187], v[224:227], v[48:51]
	v_mfma_f32_16x16x32_bf16 v[28:31], v[176:179], v[232:235], v[28:31]
	v_mfma_f32_16x16x32_bf16 v[32:35], v[184:187], v[232:235], v[32:35]
	v_mfma_f32_16x16x32_bf16 v[12:15], v[176:179], v[240:243], v[12:15]
	v_mfma_f32_16x16x32_bf16 v[16:19], v[184:187], v[240:243], v[16:19]
	s_setprio 0
	s_barrier
	s_add_i32 s58, s58, 2
	s_add_u32 s46, s46, 0x100
	s_addc_u32 s47, s47, 0
	s_add_u32 s56, s56, 0x100
	s_addc_u32 s57, s57, 0
	s_cmp_gt_u32 s58, 61
	s_cbranch_scc0 .LBB0_1319
	s_and_b64 vcc, exec, s[36:37]
	s_cbranch_vccz .LBB0_1322
	s_barrier

.LBB0_2022:
	s_add_u32 s2, s56, 0x80
	s_addc_u32 s3, s57, 0
	s_cmp_eq_u32 s43, 28
	s_cselect_b32 s61, s49, s3
	s_cselect_b32 s60, s48, s2
	s_cselect_b32 s59, s51, s7
	s_cselect_b32 s58, s50, s6
	s_add_i32 s2, 0, 0x10000
	v_add_u32_e32 v2, s2, v214
	s_add_i32 s47, 0, 0x14000
	s_waitcnt vmcnt(0)
	ds_read_b128 v[120:123], v2
	ds_read_b128 v[128:131], v2 offset:1024
	ds_read_b128 v[132:135], v2 offset:2048
	ds_read_b128 v[136:139], v2 offset:3072
	v_add_u32_e32 v2, s47, v214
	ds_read_b128 v[148:151], v2
	ds_read_b128 v[152:155], v2 offset:1024
	ds_read_b128 v[172:175], v2 offset:2048
	ds_read_b128 v[176:179], v2 offset:3072
	v_lshl_add_u64 v[194:195], s[56:57], 0, v[170:171]
	s_add_i32 m0, s20, 0xc000
	ds_read_b128 v[180:183], v215
	ds_read_b128 v[184:187], v215 offset:1024
	ds_read_b128 v[190:193], v215 offset:2048
	ds_read_b128 v[216:219], v215 offset:3072
	ds_read_b128 v[224:227], v215 offset:4096
	ds_read_b128 v[228:231], v215 offset:5120
	ds_read_b128 v[232:235], v215 offset:6144
	ds_read_b128 v[236:239], v215 offset:7168
	global_load_lds_dwordx4 v[194:195], off
	v_lshl_add_u64 v[194:195], s[56:57], 0, v[168:169]
	s_add_i32 m0, s20, 0xe000
	s_nop 0
	global_load_lds_dwordx4 v[194:195], off
	s_waitcnt vmcnt(8)
	s_waitcnt lgkmcnt(0)
	s_barrier
	s_setprio 1
	s_waitcnt lgkmcnt(0)
	v_mfma_f32_16x16x32_bf16 v[144:147], v[120:123], v[180:183], v[144:147]
	v_mfma_f32_16x16x32_bf16 v[140:143], v[132:135], v[180:183], v[140:143]
	v_mfma_f32_16x16x32_bf16 v[112:115], v[120:123], v[190:193], v[112:115]
	v_mfma_f32_16x16x32_bf16 v[108:111], v[132:135], v[190:193], v[108:111]
	v_mfma_f32_16x16x32_bf16 v[96:99], v[120:123], v[224:227], v[96:99]
	v_mfma_f32_16x16x32_bf16 v[92:95], v[132:135], v[224:227], v[92:95]
	v_mfma_f32_16x16x32_bf16 v[80:83], v[120:123], v[232:235], v[80:83]
	v_mfma_f32_16x16x32_bf16 v[76:79], v[132:135], v[232:235], v[76:79]
	s_setprio 0
	s_setprio 1
	v_mfma_f32_16x16x32_bf16 v[144:147], v[128:131], v[184:187], v[144:147]
	v_mfma_f32_16x16x32_bf16 v[140:143], v[136:139], v[184:187], v[140:143]
	v_mfma_f32_16x16x32_bf16 v[112:115], v[128:131], v[216:219], v[112:115]
	v_mfma_f32_16x16x32_bf16 v[108:111], v[136:139], v[216:219], v[108:111]
	v_mfma_f32_16x16x32_bf16 v[96:99], v[128:131], v[228:231], v[96:99]
	v_mfma_f32_16x16x32_bf16 v[92:95], v[136:139], v[228:231], v[92:95]
	v_mfma_f32_16x16x32_bf16 v[80:83], v[128:131], v[236:239], v[80:83]
	v_mfma_f32_16x16x32_bf16 v[76:79], v[136:139], v[236:239], v[76:79]
	s_setprio 0
	s_setprio 1
	v_mfma_f32_16x16x32_bf16 v[124:127], v[148:151], v[180:183], v[124:127]
	v_mfma_f32_16x16x32_bf16 v[116:119], v[172:175], v[180:183], v[116:119]
	v_mfma_f32_16x16x32_bf16 v[104:107], v[148:151], v[190:193], v[104:107]
	v_mfma_f32_16x16x32_bf16 v[100:103], v[172:175], v[190:193], v[100:103]
	v_mfma_f32_16x16x32_bf16 v[88:91], v[148:151], v[224:227], v[88:91]
	v_mfma_f32_16x16x32_bf16 v[84:87], v[172:175], v[224:227], v[84:87]
	v_mfma_f32_16x16x32_bf16 v[72:75], v[148:151], v[232:235], v[72:75]
	v_mfma_f32_16x16x32_bf16 v[68:71], v[172:175], v[232:235], v[68:71]
	s_setprio 0
	s_setprio 1
	v_mfma_f32_16x16x32_bf16 v[124:127], v[152:155], v[184:187], v[124:127]
	v_mfma_f32_16x16x32_bf16 v[116:119], v[176:179], v[184:187], v[116:119]
	v_mfma_f32_16x16x32_bf16 v[104:107], v[152:155], v[216:219], v[104:107]
	v_mfma_f32_16x16x32_bf16 v[100:103], v[176:179], v[216:219], v[100:103]
	v_mfma_f32_16x16x32_bf16 v[88:91], v[152:155], v[228:231], v[88:91]
	v_mfma_f32_16x16x32_bf16 v[84:87], v[176:179], v[228:231], v[84:87]
	v_mfma_f32_16x16x32_bf16 v[72:75], v[152:155], v[236:239], v[72:75]
	v_mfma_f32_16x16x32_bf16 v[68:71], v[176:179], v[236:239], v[68:71]
	s_setprio 0
	s_barrier
	s_add_i32 s2, s2, s19
	v_lshl_add_u64 v[194:195], s[58:59], 0, v[156:157]
	s_mov_b32 m0, s2
	ds_read_b128 v[180:183], v215 offset:16384
	ds_read_b128 v[184:187], v215 offset:17408
	ds_read_b128 v[190:193], v215 offset:18432
	ds_read_b128 v[216:219], v215 offset:19456
	ds_read_b128 v[224:227], v215 offset:20480
	ds_read_b128 v[228:231], v215 offset:21504
	ds_read_b128 v[232:235], v215 offset:22528
	ds_read_b128 v[236:239], v215 offset:23552
	global_load_lds_dwordx4 v[194:195], off
	s_add_i32 m0, s2, 0x2000
	s_add_u32 s2, s58, 0x80000
	v_lshl_add_u64 v[240:241], s[58:59], 0, v[158:159]
	s_addc_u32 s3, s59, 0
	s_add_i32 s47, s47, s19
	global_load_lds_dwordx4 v[240:241], off
	v_lshl_add_u64 v[242:243], s[2:3], 0, v[156:157]
	s_mov_b32 m0, s47
	v_lshl_add_u64 v[244:245], s[60:61], 0, v[162:163]
	global_load_lds_dwordx4 v[242:243], off
	v_lshl_add_u64 v[242:243], s[2:3], 0, v[158:159]
	s_add_i32 m0, s47, 0x2000
	s_nop 0
	global_load_lds_dwordx4 v[242:243], off
	v_lshl_add_u64 v[242:243], s[60:61], 0, v[160:161]
	s_mov_b32 m0, s20
	s_nop 0
	global_load_lds_dwordx4 v[242:243], off
	s_mov_b32 m0, s21
	s_nop 0
	global_load_lds_dwordx4 v[244:245], off
	s_waitcnt vmcnt(8)
	s_waitcnt lgkmcnt(0)
	s_barrier
	s_setprio 1
	s_waitcnt lgkmcnt(0)
	v_mfma_f32_16x16x32_bf16 v[56:59], v[120:123], v[180:183], v[56:59]
	v_mfma_f32_16x16x32_bf16 v[52:55], v[132:135], v[180:183], v[52:55]
	v_mfma_f32_16x16x32_bf16 v[40:43], v[120:123], v[190:193], v[40:43]
	v_mfma_f32_16x16x32_bf16 v[36:39], v[132:135], v[190:193], v[36:39]
	v_mfma_f32_16x16x32_bf16 v[24:27], v[120:123], v[224:227], v[24:27]
	v_mfma_f32_16x16x32_bf16 v[20:23], v[132:135], v[224:227], v[20:23]
	v_mfma_f32_16x16x32_bf16 v[8:11], v[120:123], v[232:235], v[8:11]
	v_mfma_f32_16x16x32_bf16 v[4:7], v[132:135], v[232:235], v[4:7]
	s_setprio 0
	s_setprio 1
	v_mfma_f32_16x16x32_bf16 v[56:59], v[128:131], v[184:187], v[56:59]
	v_mfma_f32_16x16x32_bf16 v[52:55], v[136:139], v[184:187], v[52:55]
	v_mfma_f32_16x16x32_bf16 v[40:43], v[128:131], v[216:219], v[40:43]
	v_mfma_f32_16x16x32_bf16 v[36:39], v[136:139], v[216:219], v[36:39]
	v_mfma_f32_16x16x32_bf16 v[24:27], v[128:131], v[228:231], v[24:27]
	v_mfma_f32_16x16x32_bf16 v[20:23], v[136:139], v[228:231], v[20:23]
	v_mfma_f32_16x16x32_bf16 v[8:11], v[128:131], v[236:239], v[8:11]
	v_mfma_f32_16x16x32_bf16 v[4:7], v[136:139], v[236:239], v[4:7]
	s_setprio 0
	s_setprio 1
	v_mfma_f32_16x16x32_bf16 v[64:67], v[148:151], v[180:183], v[64:67]
	v_mfma_f32_16x16x32_bf16 v[60:63], v[172:175], v[180:183], v[60:63]
	v_mfma_f32_16x16x32_bf16 v[48:51], v[148:151], v[190:193], v[48:51]
	v_mfma_f32_16x16x32_bf16 v[44:47], v[172:175], v[190:193], v[44:47]
	v_mfma_f32_16x16x32_bf16 v[32:35], v[148:151], v[224:227], v[32:35]
	v_mfma_f32_16x16x32_bf16 v[28:31], v[172:175], v[224:227], v[28:31]
	v_mfma_f32_16x16x32_bf16 v[16:19], v[148:151], v[232:235], v[16:19]
	v_mfma_f32_16x16x32_bf16 v[12:15], v[172:175], v[232:235], v[12:15]
	s_setprio 0
	s_setprio 1
	v_mfma_f32_16x16x32_bf16 v[64:67], v[152:155], v[184:187], v[64:67]
	v_mfma_f32_16x16x32_bf16 v[60:63], v[176:179], v[184:187], v[60:63]
	v_mfma_f32_16x16x32_bf16 v[48:51], v[152:155], v[216:219], v[48:51]
	v_mfma_f32_16x16x32_bf16 v[44:47], v[176:179], v[216:219], v[44:47]
	v_mfma_f32_16x16x32_bf16 v[32:35], v[152:155], v[228:231], v[32:35]
	v_mfma_f32_16x16x32_bf16 v[28:31], v[176:179], v[228:231], v[28:31]
	v_mfma_f32_16x16x32_bf16 v[16:19], v[152:155], v[236:239], v[16:19]
	v_mfma_f32_16x16x32_bf16 v[12:15], v[176:179], v[236:239], v[12:15]
	s_setprio 0
	s_barrier
	s_add_i32 s2, 0, 0x18000
	v_add_u32_e32 v2, s2, v214
	s_add_i32 s47, 0, 0x1c000
	ds_read_b128 v[120:123], v2
	ds_read_b128 v[128:131], v2 offset:1024
	ds_read_b128 v[132:135], v2 offset:2048
	ds_read_b128 v[136:139], v2 offset:3072
	v_add_u32_e32 v2, s47, v214
	ds_read_b128 v[148:151], v2
	ds_read_b128 v[152:155], v2 offset:1024
	ds_read_b128 v[172:175], v2 offset:2048
	ds_read_b128 v[176:179], v2 offset:3072
	s_mov_b32 m0, s22
	v_lshl_add_u64 v[246:247], s[60:61], 0, v[164:165]
	ds_read_b128 v[180:183], v215 offset:32768
	ds_read_b128 v[184:187], v215 offset:33792
	ds_read_b128 v[190:193], v215 offset:34816
	ds_read_b128 v[216:219], v215 offset:35840
	ds_read_b128 v[224:227], v215 offset:36864
	ds_read_b128 v[228:231], v215 offset:37888
	ds_read_b128 v[232:235], v215 offset:38912
	ds_read_b128 v[236:239], v215 offset:39936
	global_load_lds_dwordx4 v[246:247], off
	v_lshl_add_u64 v[246:247], s[60:61], 0, v[166:167]
	s_mov_b32 m0, s23
	s_nop 0
	global_load_lds_dwordx4 v[246:247], off
	s_waitcnt vmcnt(8)
	s_waitcnt lgkmcnt(0)
	s_barrier
	s_setprio 1
	s_waitcnt lgkmcnt(0)
	v_mfma_f32_16x16x32_bf16 v[144:147], v[120:123], v[180:183], v[144:147]
	v_mfma_f32_16x16x32_bf16 v[140:143], v[132:135], v[180:183], v[140:143]
	v_mfma_f32_16x16x32_bf16 v[112:115], v[120:123], v[190:193], v[112:115]
	v_mfma_f32_16x16x32_bf16 v[108:111], v[132:135], v[190:193], v[108:111]
	v_mfma_f32_16x16x32_bf16 v[96:99], v[120:123], v[224:227], v[96:99]
	v_mfma_f32_16x16x32_bf16 v[92:95], v[132:135], v[224:227], v[92:95]
	v_mfma_f32_16x16x32_bf16 v[80:83], v[120:123], v[232:235], v[80:83]
	v_mfma_f32_16x16x32_bf16 v[76:79], v[132:135], v[232:235], v[76:79]
	s_setprio 0
	s_setprio 1
	v_mfma_f32_16x16x32_bf16 v[144:147], v[128:131], v[184:187], v[144:147]
	v_mfma_f32_16x16x32_bf16 v[140:143], v[136:139], v[184:187], v[140:143]
	v_mfma_f32_16x16x32_bf16 v[112:115], v[128:131], v[216:219], v[112:115]
	v_mfma_f32_16x16x32_bf16 v[108:111], v[136:139], v[216:219], v[108:111]
	v_mfma_f32_16x16x32_bf16 v[96:99], v[128:131], v[228:231], v[96:99]
	v_mfma_f32_16x16x32_bf16 v[92:95], v[136:139], v[228:231], v[92:95]
	v_mfma_f32_16x16x32_bf16 v[80:83], v[128:131], v[236:239], v[80:83]
	v_mfma_f32_16x16x32_bf16 v[76:79], v[136:139], v[236:239], v[76:79]
	s_setprio 0
	s_setprio 1
	v_mfma_f32_16x16x32_bf16 v[124:127], v[148:151], v[180:183], v[124:127]
	v_mfma_f32_16x16x32_bf16 v[116:119], v[172:175], v[180:183], v[116:119]
	v_mfma_f32_16x16x32_bf16 v[104:107], v[148:151], v[190:193], v[104:107]
	v_mfma_f32_16x16x32_bf16 v[100:103], v[172:175], v[190:193], v[100:103]
	v_mfma_f32_16x16x32_bf16 v[88:91], v[148:151], v[224:227], v[88:91]
	v_mfma_f32_16x16x32_bf16 v[84:87], v[172:175], v[224:227], v[84:87]
	v_mfma_f32_16x16x32_bf16 v[72:75], v[148:151], v[232:235], v[72:75]
	v_mfma_f32_16x16x32_bf16 v[68:71], v[172:175], v[232:235], v[68:71]
	s_setprio 0
	s_setprio 1
	v_mfma_f32_16x16x32_bf16 v[124:127], v[152:155], v[184:187], v[124:127]
	v_mfma_f32_16x16x32_bf16 v[116:119], v[176:179], v[184:187], v[116:119]
	v_mfma_f32_16x16x32_bf16 v[104:107], v[152:155], v[216:219], v[104:107]
	v_mfma_f32_16x16x32_bf16 v[100:103], v[176:179], v[216:219], v[100:103]
	v_mfma_f32_16x16x32_bf16 v[88:91], v[152:155], v[228:231], v[88:91]
	v_mfma_f32_16x16x32_bf16 v[84:87], v[176:179], v[228:231], v[84:87]
	v_mfma_f32_16x16x32_bf16 v[72:75], v[152:155], v[236:239], v[72:75]
	v_mfma_f32_16x16x32_bf16 v[68:71], v[176:179], v[236:239], v[68:71]
	s_setprio 0
	s_barrier
	s_add_i32 s2, s2, s19
	v_lshl_add_u64 v[194:195], v[194:195], 0, s[30:31]
	s_mov_b32 m0, s2
	ds_read_b128 v[180:183], v215 offset:49152
	ds_read_b128 v[184:187], v215 offset:50176
	ds_read_b128 v[190:193], v215 offset:51200
	ds_read_b128 v[216:219], v215 offset:52224
	ds_read_b128 v[224:227], v215 offset:53248
	ds_read_b128 v[228:231], v215 offset:54272
	ds_read_b128 v[232:235], v215 offset:55296
	ds_read_b128 v[236:239], v215 offset:56320
	global_load_lds_dwordx4 v[194:195], off
	s_add_i32 m0, s2, 0x2000
	s_add_u32 s2, s58, 0x80080
	v_lshl_add_u64 v[194:195], v[240:241], 0, s[30:31]
	s_addc_u32 s3, s59, 0
	s_add_i32 s47, s47, s19
	global_load_lds_dwordx4 v[194:195], off
	v_lshl_add_u64 v[194:195], s[2:3], 0, v[156:157]
	s_mov_b32 m0, s47
	s_nop 0
	global_load_lds_dwordx4 v[194:195], off
	v_lshl_add_u64 v[194:195], s[2:3], 0, v[158:159]
	s_add_i32 m0, s47, 0x2000
	s_nop 0
	global_load_lds_dwordx4 v[194:195], off
	v_lshl_add_u64 v[194:195], v[242:243], 0, s[30:31]
	s_mov_b32 m0, s28
	s_nop 0
	global_load_lds_dwordx4 v[194:195], off
	v_lshl_add_u64 v[194:195], v[244:245], 0, s[30:31]
	s_mov_b32 m0, s29
	s_nop 0
	global_load_lds_dwordx4 v[194:195], off
	s_waitcnt vmcnt(8)
	s_waitcnt lgkmcnt(0)
	s_barrier
	s_setprio 1
	s_waitcnt lgkmcnt(0)
	v_mfma_f32_16x16x32_bf16 v[56:59], v[120:123], v[180:183], v[56:59]
	v_mfma_f32_16x16x32_bf16 v[52:55], v[132:135], v[180:183], v[52:55]
	v_mfma_f32_16x16x32_bf16 v[40:43], v[120:123], v[190:193], v[40:43]
	v_mfma_f32_16x16x32_bf16 v[36:39], v[132:135], v[190:193], v[36:39]
	v_mfma_f32_16x16x32_bf16 v[24:27], v[120:123], v[224:227], v[24:27]
	v_mfma_f32_16x16x32_bf16 v[20:23], v[132:135], v[224:227], v[20:23]
	v_mfma_f32_16x16x32_bf16 v[8:11], v[120:123], v[232:235], v[8:11]
	v_mfma_f32_16x16x32_bf16 v[4:7], v[132:135], v[232:235], v[4:7]
	s_setprio 0
	s_setprio 1
	v_mfma_f32_16x16x32_bf16 v[56:59], v[128:131], v[184:187], v[56:59]
	v_mfma_f32_16x16x32_bf16 v[52:55], v[136:139], v[184:187], v[52:55]
	v_mfma_f32_16x16x32_bf16 v[40:43], v[128:131], v[216:219], v[40:43]
	v_mfma_f32_16x16x32_bf16 v[36:39], v[136:139], v[216:219], v[36:39]
	v_mfma_f32_16x16x32_bf16 v[24:27], v[128:131], v[228:231], v[24:27]
	v_mfma_f32_16x16x32_bf16 v[20:23], v[136:139], v[228:231], v[20:23]
	v_mfma_f32_16x16x32_bf16 v[8:11], v[128:131], v[236:239], v[8:11]
	v_mfma_f32_16x16x32_bf16 v[4:7], v[136:139], v[236:239], v[4:7]
	s_setprio 0
	s_setprio 1
	v_mfma_f32_16x16x32_bf16 v[64:67], v[148:151], v[180:183], v[64:67]
	v_mfma_f32_16x16x32_bf16 v[60:63], v[172:175], v[180:183], v[60:63]
	v_mfma_f32_16x16x32_bf16 v[48:51], v[148:151], v[190:193], v[48:51]
	v_mfma_f32_16x16x32_bf16 v[44:47], v[172:175], v[190:193], v[44:47]
	v_mfma_f32_16x16x32_bf16 v[32:35], v[148:151], v[224:227], v[32:35]
	v_mfma_f32_16x16x32_bf16 v[28:31], v[172:175], v[224:227], v[28:31]
	v_mfma_f32_16x16x32_bf16 v[16:19], v[148:151], v[232:235], v[16:19]
	v_mfma_f32_16x16x32_bf16 v[12:15], v[172:175], v[232:235], v[12:15]
	s_setprio 0
	s_setprio 1
	v_mfma_f32_16x16x32_bf16 v[64:67], v[152:155], v[184:187], v[64:67]
	v_mfma_f32_16x16x32_bf16 v[60:63], v[176:179], v[184:187], v[60:63]
	v_mfma_f32_16x16x32_bf16 v[48:51], v[152:155], v[216:219], v[48:51]
	v_mfma_f32_16x16x32_bf16 v[44:47], v[176:179], v[216:219], v[44:47]
	v_mfma_f32_16x16x32_bf16 v[32:35], v[152:155], v[228:231], v[32:35]
	v_mfma_f32_16x16x32_bf16 v[28:31], v[176:179], v[228:231], v[28:31]
	v_mfma_f32_16x16x32_bf16 v[16:19], v[152:155], v[236:239], v[16:19]
	v_mfma_f32_16x16x32_bf16 v[12:15], v[176:179], v[236:239], v[12:15]
	s_setprio 0
	s_barrier
	s_add_i32 s43, s43, 2
	s_add_u32 s56, s56, 0x100
	s_addc_u32 s57, s57, 0
	s_add_u32 s6, s6, 0x100
	s_addc_u32 s7, s7, 0
	s_cmp_gt_u32 s43, 29
	s_cbranch_scc0 .LBB0_2022
	s_and_b64 vcc, exec, s[40:41]
	s_cbranch_vccz .LBB0_2025
	s_barrier

.LBB0_2360:
	s_add_u32 s2, s0, s56
	s_addc_u32 s3, s1, s57
	s_add_u32 s53, s2, 0x40200100
	s_addc_u32 s55, s3, 0
	s_add_u32 s58, s7, s56
	s_addc_u32 s59, s47, s57
	s_cmpk_eq_i32 s56, 0xf00
	s_cselect_b64 vcc, -1, 0
	s_and_b64 s[2:3], vcc, exec
	s_cselect_b32 s61, s37, s55
	s_cselect_b32 s60, s36, s53
	s_cselect_b32 s59, s51, s59
	s_cselect_b32 s58, s50, s58
	s_add_i32 s2, 0, 0x10000
	s_add_i32 s53, 0, 0x14000
	v_add_u32_e32 v170, s2, v154
	v_add_u32_e32 v187, s53, v154
	ds_read_b128 v[158:161], v170
	ds_read_b128 v[162:165], v170 offset:1024
	ds_read_b128 v[166:169], v170 offset:2048
	ds_read_b128 v[170:173], v170 offset:3072
	ds_read_b128 v[174:177], v187
	ds_read_b128 v[178:181], v187 offset:1024
	ds_read_b128 v[182:185], v187 offset:2048
	ds_read_b128 v[190:193], v187 offset:3072
	v_cndmask_b32_e32 v2, v142, v143, vcc
	v_cndmask_b32_e32 v186, v140, v155, vcc
	v_cndmask_b32_e32 v137, v138, v156, vcc
	v_cndmask_b32_e32 v139, v136, v157, vcc
	v_lshl_add_u64 v[194:195], v[146:147], 0, s[56:57]
	s_add_i32 m0, s21, 0xc000
	ds_read_b128 v[212:215], v141
	ds_read_b128 v[216:219], v141 offset:1024
	ds_read_b128 v[224:227], v141 offset:2048
	ds_read_b128 v[228:231], v141 offset:3072
	ds_read_b128 v[232:235], v141 offset:4096
	ds_read_b128 v[236:239], v141 offset:5120
	ds_read_b128 v[240:243], v141 offset:6144
	ds_read_b128 v[244:247], v141 offset:7168
	global_load_lds_dwordx4 v[194:195], off
	v_lshl_add_u64 v[194:195], v[144:145], 0, s[56:57]
	s_add_i32 m0, s21, 0xe000
	s_nop 0
	global_load_lds_dwordx4 v[194:195], off
	s_waitcnt vmcnt(8)
	s_waitcnt lgkmcnt(0)
	s_barrier
	s_setprio 1
	s_waitcnt lgkmcnt(0)
	v_mfma_f32_16x16x32_bf16 v[128:131], v[158:161], v[212:215], v[128:131]
	v_mfma_f32_16x16x32_bf16 v[124:127], v[166:169], v[212:215], v[124:127]
	v_mfma_f32_16x16x32_bf16 v[112:115], v[158:161], v[224:227], v[112:115]
	v_mfma_f32_16x16x32_bf16 v[108:111], v[166:169], v[224:227], v[108:111]
	v_mfma_f32_16x16x32_bf16 v[96:99], v[158:161], v[232:235], v[96:99]
	v_mfma_f32_16x16x32_bf16 v[92:95], v[166:169], v[232:235], v[92:95]
	v_mfma_f32_16x16x32_bf16 v[80:83], v[158:161], v[240:243], v[80:83]
	v_mfma_f32_16x16x32_bf16 v[76:79], v[166:169], v[240:243], v[76:79]
	s_setprio 0
	s_setprio 1
	v_mfma_f32_16x16x32_bf16 v[128:131], v[162:165], v[216:219], v[128:131]
	v_mfma_f32_16x16x32_bf16 v[124:127], v[170:173], v[216:219], v[124:127]
	v_mfma_f32_16x16x32_bf16 v[112:115], v[162:165], v[228:231], v[112:115]
	v_mfma_f32_16x16x32_bf16 v[108:111], v[170:173], v[228:231], v[108:111]
	v_mfma_f32_16x16x32_bf16 v[96:99], v[162:165], v[236:239], v[96:99]
	v_mfma_f32_16x16x32_bf16 v[92:95], v[170:173], v[236:239], v[92:95]
	v_mfma_f32_16x16x32_bf16 v[80:83], v[162:165], v[244:247], v[80:83]
	v_mfma_f32_16x16x32_bf16 v[76:79], v[170:173], v[244:247], v[76:79]
	s_setprio 0
	s_setprio 1
	v_mfma_f32_16x16x32_bf16 v[120:123], v[174:177], v[212:215], v[120:123]
	v_mfma_f32_16x16x32_bf16 v[116:119], v[182:185], v[212:215], v[116:119]
	v_mfma_f32_16x16x32_bf16 v[104:107], v[174:177], v[224:227], v[104:107]
	v_mfma_f32_16x16x32_bf16 v[100:103], v[182:185], v[224:227], v[100:103]
	v_mfma_f32_16x16x32_bf16 v[88:91], v[174:177], v[232:235], v[88:91]
	v_mfma_f32_16x16x32_bf16 v[84:87], v[182:185], v[232:235], v[84:87]
	v_mfma_f32_16x16x32_bf16 v[72:75], v[174:177], v[240:243], v[72:75]
	v_mfma_f32_16x16x32_bf16 v[68:71], v[182:185], v[240:243], v[68:71]
	s_setprio 0
	s_setprio 1
	v_mfma_f32_16x16x32_bf16 v[120:123], v[178:181], v[216:219], v[120:123]
	v_mfma_f32_16x16x32_bf16 v[116:119], v[190:193], v[216:219], v[116:119]
	v_mfma_f32_16x16x32_bf16 v[104:107], v[178:181], v[228:231], v[104:107]
	v_mfma_f32_16x16x32_bf16 v[100:103], v[190:193], v[228:231], v[100:103]
	v_mfma_f32_16x16x32_bf16 v[88:91], v[178:181], v[236:239], v[88:91]
	v_mfma_f32_16x16x32_bf16 v[84:87], v[190:193], v[236:239], v[84:87]
	v_mfma_f32_16x16x32_bf16 v[72:75], v[178:181], v[244:247], v[72:75]
	v_mfma_f32_16x16x32_bf16 v[68:71], v[190:193], v[244:247], v[68:71]
	s_setprio 0
	s_barrier
	s_add_i32 s2, s2, s20
	v_lshl_add_u64 v[194:195], s[58:59], 0, v[134:135]
	s_mov_b32 m0, s2
	ds_read_b128 v[212:215], v141 offset:16384
	ds_read_b128 v[216:219], v141 offset:17408
	ds_read_b128 v[224:227], v141 offset:18432
	ds_read_b128 v[228:231], v141 offset:19456
	ds_read_b128 v[232:235], v141 offset:20480
	ds_read_b128 v[236:239], v141 offset:21504
	ds_read_b128 v[240:243], v141 offset:22528
	ds_read_b128 v[244:247], v141 offset:23552
	global_load_lds_dwordx4 v[194:195], off
	s_add_i32 m0, s2, 0x2000
	s_add_u32 s2, s58, 0x80000
	v_lshl_add_u64 v[248:249], s[58:59], 0, v[132:133]
	s_addc_u32 s3, s59, 0
	s_add_i32 s53, s53, s20
	global_load_lds_dwordx4 v[248:249], off
	v_lshl_add_u64 v[250:251], s[2:3], 0, v[134:135]
	s_mov_b32 m0, s53
	v_mov_b32_e32 v187, v3
	global_load_lds_dwordx4 v[250:251], off
	v_lshl_add_u64 v[250:251], s[2:3], 0, v[132:133]
	s_add_i32 m0, s53, 0x2000
	s_nop 0
	global_load_lds_dwordx4 v[250:251], off
	s_mov_b32 m0, s21
	v_lshl_add_u64 v[250:251], s[60:61], 0, v[2:3]
	global_load_lds_dwordx4 v2, s[60:61]
	s_mov_b32 m0, s22
	s_nop 0
	global_load_lds_dwordx4 v186, s[60:61]
	s_waitcnt vmcnt(8)
	s_waitcnt lgkmcnt(0)
	v_lshl_add_u64 v[186:187], s[60:61], 0, v[186:187]
	s_barrier
	s_setprio 1
	s_waitcnt lgkmcnt(0)
	s_cmp_eq_u32 s6, 8
	s_cbranch_scc1 .Lpadskip_p8_1
	v_mfma_f32_16x16x32_bf16 v[64:67], v[158:161], v[212:215], v[64:67]
	v_mfma_f32_16x16x32_bf16 v[56:59], v[166:169], v[212:215], v[56:59]
	v_mfma_f32_16x16x32_bf16 v[48:51], v[158:161], v[224:227], v[48:51]
	v_mfma_f32_16x16x32_bf16 v[40:43], v[166:169], v[224:227], v[40:43]
	v_mfma_f32_16x16x32_bf16 v[28:31], v[158:161], v[232:235], v[28:31]
	v_mfma_f32_16x16x32_bf16 v[20:23], v[166:169], v[232:235], v[20:23]
	v_mfma_f32_16x16x32_bf16 v[12:15], v[158:161], v[240:243], v[12:15]
	v_mfma_f32_16x16x32_bf16 v[4:7], v[166:169], v[240:243], v[4:7]
	s_setprio 0
	s_setprio 1
	v_mfma_f32_16x16x32_bf16 v[64:67], v[162:165], v[216:219], v[64:67]
	v_mfma_f32_16x16x32_bf16 v[56:59], v[170:173], v[216:219], v[56:59]
	v_mfma_f32_16x16x32_bf16 v[48:51], v[162:165], v[228:231], v[48:51]
	v_mfma_f32_16x16x32_bf16 v[40:43], v[170:173], v[228:231], v[40:43]
	v_mfma_f32_16x16x32_bf16 v[28:31], v[162:165], v[236:239], v[28:31]
	v_mfma_f32_16x16x32_bf16 v[20:23], v[170:173], v[236:239], v[20:23]
	v_mfma_f32_16x16x32_bf16 v[12:15], v[162:165], v[244:247], v[12:15]
	v_mfma_f32_16x16x32_bf16 v[4:7], v[170:173], v[244:247], v[4:7]
	s_setprio 0
	s_setprio 1
	v_mfma_f32_16x16x32_bf16 v[60:63], v[174:177], v[212:215], v[60:63]
	v_mfma_f32_16x16x32_bf16 v[52:55], v[182:185], v[212:215], v[52:55]
	v_mfma_f32_16x16x32_bf16 v[44:47], v[174:177], v[224:227], v[44:47]
	v_mfma_f32_16x16x32_bf16 v[32:35], v[182:185], v[224:227], v[32:35]
	v_mfma_f32_16x16x32_bf16 v[36:39], v[174:177], v[232:235], v[36:39]
	v_mfma_f32_16x16x32_bf16 v[24:27], v[182:185], v[232:235], v[24:27]
	v_mfma_f32_16x16x32_bf16 v[16:19], v[174:177], v[240:243], v[16:19]
	v_mfma_f32_16x16x32_bf16 v[8:11], v[182:185], v[240:243], v[8:11]
	s_setprio 0
	s_setprio 1
	v_mfma_f32_16x16x32_bf16 v[60:63], v[178:181], v[216:219], v[60:63]
	v_mfma_f32_16x16x32_bf16 v[52:55], v[190:193], v[216:219], v[52:55]
	v_mfma_f32_16x16x32_bf16 v[44:47], v[178:181], v[228:231], v[44:47]
	v_mfma_f32_16x16x32_bf16 v[32:35], v[190:193], v[228:231], v[32:35]
	v_mfma_f32_16x16x32_bf16 v[36:39], v[178:181], v[236:239], v[36:39]
	v_mfma_f32_16x16x32_bf16 v[24:27], v[190:193], v[236:239], v[24:27]
	v_mfma_f32_16x16x32_bf16 v[16:19], v[178:181], v[244:247], v[16:19]
	v_mfma_f32_16x16x32_bf16 v[8:11], v[190:193], v[244:247], v[8:11]
.Lpadskip_p8_1:
	s_setprio 0
	s_barrier
	s_add_i32 s2, 0, 0x18000
	v_add_u32_e32 v2, s2, v154
	s_add_i32 s53, 0, 0x1c000
	ds_read_b128 v[158:161], v2
	ds_read_b128 v[162:165], v2 offset:1024
	ds_read_b128 v[166:169], v2 offset:2048
	ds_read_b128 v[170:173], v2 offset:3072
	v_add_u32_e32 v2, s53, v154
	ds_read_b128 v[174:177], v2
	ds_read_b128 v[178:181], v2 offset:1024
	ds_read_b128 v[182:185], v2 offset:2048
	ds_read_b128 v[190:193], v2 offset:3072
	s_mov_b32 m0, s23
	ds_read_b128 v[212:215], v141 offset:32768
	ds_read_b128 v[216:219], v141 offset:33792
	ds_read_b128 v[224:227], v141 offset:34816
	ds_read_b128 v[228:231], v141 offset:35840
	ds_read_b128 v[232:235], v141 offset:36864
	ds_read_b128 v[236:239], v141 offset:37888
	ds_read_b128 v[240:243], v141 offset:38912
	ds_read_b128 v[244:247], v141 offset:39936
	global_load_lds_dwordx4 v137, s[60:61]
	s_mov_b32 m0, s24
	s_nop 0
	global_load_lds_dwordx4 v139, s[60:61]
	s_waitcnt vmcnt(8)
	s_waitcnt lgkmcnt(0)
	s_barrier
	s_setprio 1
	s_waitcnt lgkmcnt(0)
	v_mfma_f32_16x16x32_bf16 v[128:131], v[158:161], v[212:215], v[128:131]
	v_mfma_f32_16x16x32_bf16 v[124:127], v[166:169], v[212:215], v[124:127]
	v_mfma_f32_16x16x32_bf16 v[112:115], v[158:161], v[224:227], v[112:115]
	v_mfma_f32_16x16x32_bf16 v[108:111], v[166:169], v[224:227], v[108:111]
	v_mfma_f32_16x16x32_bf16 v[96:99], v[158:161], v[232:235], v[96:99]
	v_mfma_f32_16x16x32_bf16 v[92:95], v[166:169], v[232:235], v[92:95]
	v_mfma_f32_16x16x32_bf16 v[80:83], v[158:161], v[240:243], v[80:83]
	v_mfma_f32_16x16x32_bf16 v[76:79], v[166:169], v[240:243], v[76:79]
	s_setprio 0
	s_setprio 1
	v_mfma_f32_16x16x32_bf16 v[128:131], v[162:165], v[216:219], v[128:131]
	v_mfma_f32_16x16x32_bf16 v[124:127], v[170:173], v[216:219], v[124:127]
	v_mfma_f32_16x16x32_bf16 v[112:115], v[162:165], v[228:231], v[112:115]
	v_mfma_f32_16x16x32_bf16 v[108:111], v[170:173], v[228:231], v[108:111]
	v_mfma_f32_16x16x32_bf16 v[96:99], v[162:165], v[236:239], v[96:99]
	v_mfma_f32_16x16x32_bf16 v[92:95], v[170:173], v[236:239], v[92:95]
	v_mfma_f32_16x16x32_bf16 v[80:83], v[162:165], v[244:247], v[80:83]
	v_mfma_f32_16x16x32_bf16 v[76:79], v[170:173], v[244:247], v[76:79]
	s_setprio 0
	s_setprio 1
	v_mfma_f32_16x16x32_bf16 v[120:123], v[174:177], v[212:215], v[120:123]
	v_mfma_f32_16x16x32_bf16 v[116:119], v[182:185], v[212:215], v[116:119]
	v_mfma_f32_16x16x32_bf16 v[104:107], v[174:177], v[224:227], v[104:107]
	v_mfma_f32_16x16x32_bf16 v[100:103], v[182:185], v[224:227], v[100:103]
	v_mfma_f32_16x16x32_bf16 v[88:91], v[174:177], v[232:235], v[88:91]
	v_mfma_f32_16x16x32_bf16 v[84:87], v[182:185], v[232:235], v[84:87]
	v_mfma_f32_16x16x32_bf16 v[72:75], v[174:177], v[240:243], v[72:75]
	v_mfma_f32_16x16x32_bf16 v[68:71], v[182:185], v[240:243], v[68:71]
	s_setprio 0
	s_setprio 1
	v_mfma_f32_16x16x32_bf16 v[120:123], v[178:181], v[216:219], v[120:123]
	v_mfma_f32_16x16x32_bf16 v[116:119], v[190:193], v[216:219], v[116:119]
	v_mfma_f32_16x16x32_bf16 v[104:107], v[178:181], v[228:231], v[104:107]
	v_mfma_f32_16x16x32_bf16 v[100:103], v[190:193], v[228:231], v[100:103]
	v_mfma_f32_16x16x32_bf16 v[88:91], v[178:181], v[236:239], v[88:91]
	v_mfma_f32_16x16x32_bf16 v[84:87], v[190:193], v[236:239], v[84:87]
	v_mfma_f32_16x16x32_bf16 v[72:75], v[178:181], v[244:247], v[72:75]
	v_mfma_f32_16x16x32_bf16 v[68:71], v[190:193], v[244:247], v[68:71]
	s_setprio 0
	s_barrier
	s_add_i32 s2, s2, s20
	v_lshl_add_u64 v[194:195], v[194:195], 0, s[30:31]
	s_mov_b32 m0, s2
	ds_read_b128 v[212:215], v141 offset:49152
	ds_read_b128 v[216:219], v141 offset:50176
	ds_read_b128 v[224:227], v141 offset:51200
	ds_read_b128 v[228:231], v141 offset:52224
	ds_read_b128 v[232:235], v141 offset:53248
	ds_read_b128 v[236:239], v141 offset:54272
	ds_read_b128 v[240:243], v141 offset:55296
	ds_read_b128 v[244:247], v141 offset:56320
	global_load_lds_dwordx4 v[194:195], off
	s_add_i32 m0, s2, 0x2000
	s_add_u32 s2, s58, 0x80080
	v_lshl_add_u64 v[194:195], v[248:249], 0, s[30:31]
	s_addc_u32 s3, s59, 0
	s_add_i32 s53, s53, s20
	global_load_lds_dwordx4 v[194:195], off
	v_lshl_add_u64 v[194:195], s[2:3], 0, v[134:135]
	s_mov_b32 m0, s53
	v_lshl_add_u64 v[186:187], v[186:187], 0, s[30:31]
	global_load_lds_dwordx4 v[194:195], off
	v_lshl_add_u64 v[194:195], s[2:3], 0, v[132:133]
	s_add_i32 m0, s53, 0x2000
	s_nop 0
	global_load_lds_dwordx4 v[194:195], off
	v_lshl_add_u64 v[194:195], v[250:251], 0, s[30:31]
	s_mov_b32 m0, s26
	s_nop 0
	global_load_lds_dwordx4 v[194:195], off
	s_mov_b32 m0, s27
	s_nop 0
	global_load_lds_dwordx4 v[186:187], off
	s_waitcnt vmcnt(8)
	s_waitcnt lgkmcnt(0)
	s_barrier
	s_setprio 1
	s_waitcnt lgkmcnt(0)
	s_cmp_eq_u32 s6, 8
	s_cbranch_scc1 .Lpadskip_p8_3
	v_mfma_f32_16x16x32_bf16 v[64:67], v[158:161], v[212:215], v[64:67]
	v_mfma_f32_16x16x32_bf16 v[56:59], v[166:169], v[212:215], v[56:59]
	v_mfma_f32_16x16x32_bf16 v[48:51], v[158:161], v[224:227], v[48:51]
	v_mfma_f32_16x16x32_bf16 v[40:43], v[166:169], v[224:227], v[40:43]
	v_mfma_f32_16x16x32_bf16 v[28:31], v[158:161], v[232:235], v[28:31]
	v_mfma_f32_16x16x32_bf16 v[20:23], v[166:169], v[232:235], v[20:23]
	v_mfma_f32_16x16x32_bf16 v[12:15], v[158:161], v[240:243], v[12:15]
	v_mfma_f32_16x16x32_bf16 v[4:7], v[166:169], v[240:243], v[4:7]
	s_setprio 0
	s_setprio 1
	v_mfma_f32_16x16x32_bf16 v[64:67], v[162:165], v[216:219], v[64:67]
	v_mfma_f32_16x16x32_bf16 v[56:59], v[170:173], v[216:219], v[56:59]
	v_mfma_f32_16x16x32_bf16 v[48:51], v[162:165], v[228:231], v[48:51]
	v_mfma_f32_16x16x32_bf16 v[40:43], v[170:173], v[228:231], v[40:43]
	v_mfma_f32_16x16x32_bf16 v[28:31], v[162:165], v[236:239], v[28:31]
	v_mfma_f32_16x16x32_bf16 v[20:23], v[170:173], v[236:239], v[20:23]
	v_mfma_f32_16x16x32_bf16 v[12:15], v[162:165], v[244:247], v[12:15]
	v_mfma_f32_16x16x32_bf16 v[4:7], v[170:173], v[244:247], v[4:7]
	s_setprio 0
	s_setprio 1
	v_mfma_f32_16x16x32_bf16 v[60:63], v[174:177], v[212:215], v[60:63]
	v_mfma_f32_16x16x32_bf16 v[52:55], v[182:185], v[212:215], v[52:55]
	v_mfma_f32_16x16x32_bf16 v[44:47], v[174:177], v[224:227], v[44:47]
	v_mfma_f32_16x16x32_bf16 v[32:35], v[182:185], v[224:227], v[32:35]
	v_mfma_f32_16x16x32_bf16 v[36:39], v[174:177], v[232:235], v[36:39]
	v_mfma_f32_16x16x32_bf16 v[24:27], v[182:185], v[232:235], v[24:27]
	v_mfma_f32_16x16x32_bf16 v[16:19], v[174:177], v[240:243], v[16:19]
	v_mfma_f32_16x16x32_bf16 v[8:11], v[182:185], v[240:243], v[8:11]
	s_setprio 0
	s_setprio 1
	v_mfma_f32_16x16x32_bf16 v[60:63], v[178:181], v[216:219], v[60:63]
	v_mfma_f32_16x16x32_bf16 v[52:55], v[190:193], v[216:219], v[52:55]
	v_mfma_f32_16x16x32_bf16 v[44:47], v[178:181], v[228:231], v[44:47]
	v_mfma_f32_16x16x32_bf16 v[32:35], v[190:193], v[228:231], v[32:35]
	v_mfma_f32_16x16x32_bf16 v[36:39], v[178:181], v[236:239], v[36:39]
	v_mfma_f32_16x16x32_bf16 v[24:27], v[190:193], v[236:239], v[24:27]
	v_mfma_f32_16x16x32_bf16 v[16:19], v[178:181], v[244:247], v[16:19]
	v_mfma_f32_16x16x32_bf16 v[8:11], v[190:193], v[244:247], v[8:11]

.LBB0_2430:
	s_add_u32 s2, s56, 0x80
	s_addc_u32 s3, s57, 0
	s_cmp_eq_u32 s41, 28
	s_cselect_b32 s61, s51, s3
	s_cselect_b32 s60, s50, s2
	s_cselect_b32 s59, s55, s7
	s_cselect_b32 s58, s54, s6
	s_add_i32 s2, 0, 0x10000
	v_add_u32_e32 v146, s2, v150
	s_add_i32 s43, 0, 0x14000
	ds_read_b128 v[152:155], v146
	ds_read_b128 v[156:159], v146 offset:1024
	ds_read_b128 v[160:163], v146 offset:2048
	ds_read_b128 v[164:167], v146 offset:3072
	v_add_u32_e32 v146, s43, v150
	ds_read_b128 v[168:171], v146
	ds_read_b128 v[172:175], v146 offset:1024
	ds_read_b128 v[176:179], v146 offset:2048
	ds_read_b128 v[180:183], v146 offset:3072
	v_lshl_add_u64 v[146:147], s[56:57], 0, v[144:145]
	s_add_i32 m0, s23, 0xc000
	ds_read_b128 v[184:187], v151
	ds_read_b128 v[190:193], v151 offset:1024
	ds_read_b128 v[212:215], v151 offset:2048
	ds_read_b128 v[216:219], v151 offset:3072
	ds_read_b128 v[224:227], v151 offset:4096
	ds_read_b128 v[228:231], v151 offset:5120
	ds_read_b128 v[232:235], v151 offset:6144
	ds_read_b128 v[236:239], v151 offset:7168
	global_load_lds_dwordx4 v[146:147], off
	v_lshl_add_u64 v[146:147], s[56:57], 0, v[142:143]
	s_add_i32 m0, s23, 0xe000
	s_nop 0
	global_load_lds_dwordx4 v[146:147], off
	s_waitcnt vmcnt(8)
	s_waitcnt lgkmcnt(0)
	s_barrier
	s_setprio 1
	s_waitcnt lgkmcnt(0)
	v_mfma_f32_16x16x32_bf16 v[128:131], v[152:155], v[184:187], v[128:131]
	v_mfma_f32_16x16x32_bf16 v[124:127], v[160:163], v[184:187], v[124:127]
	v_mfma_f32_16x16x32_bf16 v[120:123], v[152:155], v[212:215], v[120:123]
	v_mfma_f32_16x16x32_bf16 v[116:119], v[160:163], v[212:215], v[116:119]
	v_mfma_f32_16x16x32_bf16 v[104:107], v[152:155], v[224:227], v[104:107]
	v_mfma_f32_16x16x32_bf16 v[100:103], v[160:163], v[224:227], v[100:103]
	v_mfma_f32_16x16x32_bf16 v[88:91], v[152:155], v[232:235], v[88:91]
	v_mfma_f32_16x16x32_bf16 v[84:87], v[160:163], v[232:235], v[84:87]
	s_setprio 0
	s_setprio 1
	v_mfma_f32_16x16x32_bf16 v[128:131], v[156:159], v[190:193], v[128:131]
	v_mfma_f32_16x16x32_bf16 v[124:127], v[164:167], v[190:193], v[124:127]
	v_mfma_f32_16x16x32_bf16 v[120:123], v[156:159], v[216:219], v[120:123]
	v_mfma_f32_16x16x32_bf16 v[116:119], v[164:167], v[216:219], v[116:119]
	v_mfma_f32_16x16x32_bf16 v[104:107], v[156:159], v[228:231], v[104:107]
	v_mfma_f32_16x16x32_bf16 v[100:103], v[164:167], v[228:231], v[100:103]
	v_mfma_f32_16x16x32_bf16 v[88:91], v[156:159], v[236:239], v[88:91]
	v_mfma_f32_16x16x32_bf16 v[84:87], v[164:167], v[236:239], v[84:87]
	s_setprio 0
	s_setprio 1
	v_mfma_f32_16x16x32_bf16 v[112:115], v[168:171], v[184:187], v[112:115]
	v_mfma_f32_16x16x32_bf16 v[108:111], v[176:179], v[184:187], v[108:111]
	v_mfma_f32_16x16x32_bf16 v[96:99], v[168:171], v[212:215], v[96:99]
	v_mfma_f32_16x16x32_bf16 v[92:95], v[176:179], v[212:215], v[92:95]
	v_mfma_f32_16x16x32_bf16 v[80:83], v[168:171], v[224:227], v[80:83]
	v_mfma_f32_16x16x32_bf16 v[72:75], v[176:179], v[224:227], v[72:75]
	v_mfma_f32_16x16x32_bf16 v[56:59], v[168:171], v[232:235], v[56:59]
	v_mfma_f32_16x16x32_bf16 v[52:55], v[176:179], v[232:235], v[52:55]
	s_setprio 0
	s_setprio 1
	v_mfma_f32_16x16x32_bf16 v[112:115], v[172:175], v[190:193], v[112:115]
	v_mfma_f32_16x16x32_bf16 v[108:111], v[180:183], v[190:193], v[108:111]
	v_mfma_f32_16x16x32_bf16 v[96:99], v[172:175], v[216:219], v[96:99]
	v_mfma_f32_16x16x32_bf16 v[92:95], v[180:183], v[216:219], v[92:95]
	v_mfma_f32_16x16x32_bf16 v[80:83], v[172:175], v[228:231], v[80:83]
	v_mfma_f32_16x16x32_bf16 v[72:75], v[180:183], v[228:231], v[72:75]
	v_mfma_f32_16x16x32_bf16 v[56:59], v[172:175], v[236:239], v[56:59]
	v_mfma_f32_16x16x32_bf16 v[52:55], v[180:183], v[236:239], v[52:55]
	s_setprio 0
	s_barrier
	s_add_i32 s2, s2, s21
	v_lshl_add_u64 v[146:147], s[58:59], 0, v[2:3]
	s_mov_b32 m0, s2
	ds_read_b128 v[184:187], v151 offset:16384
	ds_read_b128 v[190:193], v151 offset:17408
	ds_read_b128 v[212:215], v151 offset:18432
	ds_read_b128 v[216:219], v151 offset:19456
	ds_read_b128 v[224:227], v151 offset:20480
	ds_read_b128 v[228:231], v151 offset:21504
	ds_read_b128 v[232:235], v151 offset:22528
	ds_read_b128 v[236:239], v151 offset:23552
	global_load_lds_dwordx4 v[146:147], off
	s_add_i32 m0, s2, 0x2000
	s_add_u32 s2, s58, 0x80000
	v_lshl_add_u64 v[194:195], s[58:59], 0, v[132:133]
	s_addc_u32 s3, s59, 0
	s_add_i32 s43, s43, s21
	global_load_lds_dwordx4 v[194:195], off
	v_lshl_add_u64 v[240:241], s[2:3], 0, v[2:3]
	s_mov_b32 m0, s43
	v_lshl_add_u64 v[242:243], s[60:61], 0, v[136:137]
	global_load_lds_dwordx4 v[240:241], off
	v_lshl_add_u64 v[240:241], s[2:3], 0, v[132:133]
	s_add_i32 m0, s43, 0x2000
	s_nop 0
	global_load_lds_dwordx4 v[240:241], off
	v_lshl_add_u64 v[240:241], s[60:61], 0, v[134:135]
	s_mov_b32 m0, s23
	s_nop 0
	global_load_lds_dwordx4 v[240:241], off
	s_mov_b32 m0, s24
	s_nop 0
	global_load_lds_dwordx4 v[242:243], off
	s_waitcnt vmcnt(8)
	s_waitcnt lgkmcnt(0)
	s_barrier
	s_setprio 1
	s_waitcnt lgkmcnt(0)
	s_cmp_eq_u32 s36, 8
	s_cbranch_scc1 .Lpadskip_p9_1
	v_mfma_f32_16x16x32_bf16 v[36:39], v[152:155], v[184:187], v[36:39]
	v_mfma_f32_16x16x32_bf16 v[28:31], v[160:163], v[184:187], v[28:31]
	v_mfma_f32_16x16x32_bf16 v[24:27], v[152:155], v[212:215], v[24:27]
	v_mfma_f32_16x16x32_bf16 v[20:23], v[160:163], v[212:215], v[20:23]
	v_mfma_f32_16x16x32_bf16 v[16:19], v[152:155], v[224:227], v[16:19]
	v_mfma_f32_16x16x32_bf16 v[12:15], v[160:163], v[224:227], v[12:15]
	v_mfma_f32_16x16x32_bf16 v[8:11], v[152:155], v[232:235], v[8:11]
	v_mfma_f32_16x16x32_bf16 v[4:7], v[160:163], v[232:235], v[4:7]
	s_setprio 0
	s_setprio 1
	v_mfma_f32_16x16x32_bf16 v[36:39], v[156:159], v[190:193], v[36:39]
	v_mfma_f32_16x16x32_bf16 v[28:31], v[164:167], v[190:193], v[28:31]
	v_mfma_f32_16x16x32_bf16 v[24:27], v[156:159], v[216:219], v[24:27]
	v_mfma_f32_16x16x32_bf16 v[20:23], v[164:167], v[216:219], v[20:23]
	v_mfma_f32_16x16x32_bf16 v[16:19], v[156:159], v[228:231], v[16:19]
	v_mfma_f32_16x16x32_bf16 v[12:15], v[164:167], v[228:231], v[12:15]
	v_mfma_f32_16x16x32_bf16 v[8:11], v[156:159], v[236:239], v[8:11]
	v_mfma_f32_16x16x32_bf16 v[4:7], v[164:167], v[236:239], v[4:7]
	s_setprio 0
	s_setprio 1
	v_mfma_f32_16x16x32_bf16 v[68:71], v[168:171], v[184:187], v[68:71]
	v_mfma_f32_16x16x32_bf16 v[76:79], v[176:179], v[184:187], v[76:79]
	v_mfma_f32_16x16x32_bf16 v[60:63], v[168:171], v[212:215], v[60:63]
	v_mfma_f32_16x16x32_bf16 v[64:67], v[176:179], v[212:215], v[64:67]
	v_mfma_f32_16x16x32_bf16 v[44:47], v[168:171], v[224:227], v[44:47]
	v_mfma_f32_16x16x32_bf16 v[48:51], v[176:179], v[224:227], v[48:51]
	v_mfma_f32_16x16x32_bf16 v[32:35], v[168:171], v[232:235], v[32:35]
	v_mfma_f32_16x16x32_bf16 v[40:43], v[176:179], v[232:235], v[40:43]
	s_setprio 0
	s_setprio 1
	v_mfma_f32_16x16x32_bf16 v[68:71], v[172:175], v[190:193], v[68:71]
	v_mfma_f32_16x16x32_bf16 v[76:79], v[180:183], v[190:193], v[76:79]
	v_mfma_f32_16x16x32_bf16 v[60:63], v[172:175], v[216:219], v[60:63]
	v_mfma_f32_16x16x32_bf16 v[64:67], v[180:183], v[216:219], v[64:67]
	v_mfma_f32_16x16x32_bf16 v[44:47], v[172:175], v[228:231], v[44:47]
	v_mfma_f32_16x16x32_bf16 v[48:51], v[180:183], v[228:231], v[48:51]
	v_mfma_f32_16x16x32_bf16 v[32:35], v[172:175], v[236:239], v[32:35]
	v_mfma_f32_16x16x32_bf16 v[40:43], v[180:183], v[236:239], v[40:43]
.Lpadskip_p9_1:
	s_setprio 0
	s_barrier
	s_add_i32 s2, 0, 0x18000
	s_add_i32 s43, 0, 0x1c000
	v_add_u32_e32 v164, s2, v150
	v_add_u32_e32 v180, s43, v150
	ds_read_b128 v[152:155], v164
	ds_read_b128 v[156:159], v164 offset:1024
	ds_read_b128 v[160:163], v164 offset:2048
	ds_read_b128 v[164:167], v164 offset:3072
	ds_read_b128 v[168:171], v180
	ds_read_b128 v[172:175], v180 offset:1024
	ds_read_b128 v[176:179], v180 offset:2048
	ds_read_b128 v[180:183], v180 offset:3072
	s_mov_b32 m0, s25
	v_lshl_add_u64 v[244:245], s[60:61], 0, v[138:139]
	ds_read_b128 v[184:187], v151 offset:32768
	ds_read_b128 v[190:193], v151 offset:33792
	ds_read_b128 v[212:215], v151 offset:34816
	ds_read_b128 v[216:219], v151 offset:35840
	ds_read_b128 v[224:227], v151 offset:36864
	ds_read_b128 v[228:231], v151 offset:37888
	ds_read_b128 v[232:235], v151 offset:38912
	ds_read_b128 v[236:239], v151 offset:39936
	global_load_lds_dwordx4 v[244:245], off
	v_lshl_add_u64 v[244:245], s[60:61], 0, v[140:141]
	s_mov_b32 m0, s26
	s_nop 0
	global_load_lds_dwordx4 v[244:245], off
	s_waitcnt vmcnt(8)
	s_waitcnt lgkmcnt(0)
	s_barrier
	s_setprio 1
	s_waitcnt lgkmcnt(0)
	v_mfma_f32_16x16x32_bf16 v[128:131], v[152:155], v[184:187], v[128:131]
	v_mfma_f32_16x16x32_bf16 v[124:127], v[160:163], v[184:187], v[124:127]
	v_mfma_f32_16x16x32_bf16 v[120:123], v[152:155], v[212:215], v[120:123]
	v_mfma_f32_16x16x32_bf16 v[116:119], v[160:163], v[212:215], v[116:119]
	v_mfma_f32_16x16x32_bf16 v[104:107], v[152:155], v[224:227], v[104:107]
	v_mfma_f32_16x16x32_bf16 v[100:103], v[160:163], v[224:227], v[100:103]
	v_mfma_f32_16x16x32_bf16 v[88:91], v[152:155], v[232:235], v[88:91]
	v_mfma_f32_16x16x32_bf16 v[84:87], v[160:163], v[232:235], v[84:87]
	s_setprio 0
	s_setprio 1
	v_mfma_f32_16x16x32_bf16 v[128:131], v[156:159], v[190:193], v[128:131]
	v_mfma_f32_16x16x32_bf16 v[124:127], v[164:167], v[190:193], v[124:127]
	v_mfma_f32_16x16x32_bf16 v[120:123], v[156:159], v[216:219], v[120:123]
	v_mfma_f32_16x16x32_bf16 v[116:119], v[164:167], v[216:219], v[116:119]
	v_mfma_f32_16x16x32_bf16 v[104:107], v[156:159], v[228:231], v[104:107]
	v_mfma_f32_16x16x32_bf16 v[100:103], v[164:167], v[228:231], v[100:103]
	v_mfma_f32_16x16x32_bf16 v[88:91], v[156:159], v[236:239], v[88:91]
	v_mfma_f32_16x16x32_bf16 v[84:87], v[164:167], v[236:239], v[84:87]
	s_setprio 0
	s_setprio 1
	v_mfma_f32_16x16x32_bf16 v[112:115], v[168:171], v[184:187], v[112:115]
	v_mfma_f32_16x16x32_bf16 v[108:111], v[176:179], v[184:187], v[108:111]
	v_mfma_f32_16x16x32_bf16 v[96:99], v[168:171], v[212:215], v[96:99]
	v_mfma_f32_16x16x32_bf16 v[92:95], v[176:179], v[212:215], v[92:95]
	v_mfma_f32_16x16x32_bf16 v[80:83], v[168:171], v[224:227], v[80:83]
	v_mfma_f32_16x16x32_bf16 v[72:75], v[176:179], v[224:227], v[72:75]
	v_mfma_f32_16x16x32_bf16 v[56:59], v[168:171], v[232:235], v[56:59]
	v_mfma_f32_16x16x32_bf16 v[52:55], v[176:179], v[232:235], v[52:55]
	s_setprio 0
	s_setprio 1
	v_mfma_f32_16x16x32_bf16 v[112:115], v[172:175], v[190:193], v[112:115]
	v_mfma_f32_16x16x32_bf16 v[108:111], v[180:183], v[190:193], v[108:111]
	v_mfma_f32_16x16x32_bf16 v[96:99], v[172:175], v[216:219], v[96:99]
	v_mfma_f32_16x16x32_bf16 v[92:95], v[180:183], v[216:219], v[92:95]
	v_mfma_f32_16x16x32_bf16 v[80:83], v[172:175], v[228:231], v[80:83]
	v_mfma_f32_16x16x32_bf16 v[72:75], v[180:183], v[228:231], v[72:75]
	v_mfma_f32_16x16x32_bf16 v[56:59], v[172:175], v[236:239], v[56:59]
	v_mfma_f32_16x16x32_bf16 v[52:55], v[180:183], v[236:239], v[52:55]
	s_setprio 0
	s_barrier
	s_add_i32 s2, s2, s21
	v_lshl_add_u64 v[146:147], v[146:147], 0, s[30:31]
	s_mov_b32 m0, s2
	ds_read_b128 v[184:187], v151 offset:49152
	ds_read_b128 v[190:193], v151 offset:50176
	ds_read_b128 v[212:215], v151 offset:51200
	ds_read_b128 v[216:219], v151 offset:52224
	ds_read_b128 v[224:227], v151 offset:53248
	ds_read_b128 v[228:231], v151 offset:54272
	ds_read_b128 v[232:235], v151 offset:55296
	ds_read_b128 v[236:239], v151 offset:56320
	global_load_lds_dwordx4 v[146:147], off
	s_add_i32 m0, s2, 0x2000
	s_add_u32 s2, s58, 0x80080
	v_lshl_add_u64 v[146:147], v[194:195], 0, s[30:31]
	s_addc_u32 s3, s59, 0
	s_add_i32 s43, s43, s21
	global_load_lds_dwordx4 v[146:147], off
	v_lshl_add_u64 v[146:147], s[2:3], 0, v[2:3]
	s_mov_b32 m0, s43
	s_nop 0
	global_load_lds_dwordx4 v[146:147], off
	v_lshl_add_u64 v[146:147], s[2:3], 0, v[132:133]
	s_add_i32 m0, s43, 0x2000
	s_nop 0
	global_load_lds_dwordx4 v[146:147], off
	v_lshl_add_u64 v[146:147], v[240:241], 0, s[30:31]
	s_mov_b32 m0, s28
	s_nop 0
	global_load_lds_dwordx4 v[146:147], off
	v_lshl_add_u64 v[146:147], v[242:243], 0, s[30:31]
	s_mov_b32 m0, s29
	s_nop 0
	global_load_lds_dwordx4 v[146:147], off
	s_waitcnt vmcnt(8)
	s_waitcnt lgkmcnt(0)
	s_barrier
	s_setprio 1
	s_waitcnt lgkmcnt(0)
	s_cmp_eq_u32 s36, 8
	s_cbranch_scc1 .Lpadskip_p9_3
	v_mfma_f32_16x16x32_bf16 v[36:39], v[152:155], v[184:187], v[36:39]
	v_mfma_f32_16x16x32_bf16 v[28:31], v[160:163], v[184:187], v[28:31]
	v_mfma_f32_16x16x32_bf16 v[24:27], v[152:155], v[212:215], v[24:27]
	v_mfma_f32_16x16x32_bf16 v[20:23], v[160:163], v[212:215], v[20:23]
	v_mfma_f32_16x16x32_bf16 v[16:19], v[152:155], v[224:227], v[16:19]
	v_mfma_f32_16x16x32_bf16 v[12:15], v[160:163], v[224:227], v[12:15]
	v_mfma_f32_16x16x32_bf16 v[8:11], v[152:155], v[232:235], v[8:11]
	v_mfma_f32_16x16x32_bf16 v[4:7], v[160:163], v[232:235], v[4:7]
	s_setprio 0
	s_setprio 1
	v_mfma_f32_16x16x32_bf16 v[36:39], v[156:159], v[190:193], v[36:39]
	v_mfma_f32_16x16x32_bf16 v[28:31], v[164:167], v[190:193], v[28:31]
	v_mfma_f32_16x16x32_bf16 v[24:27], v[156:159], v[216:219], v[24:27]
	v_mfma_f32_16x16x32_bf16 v[20:23], v[164:167], v[216:219], v[20:23]
	v_mfma_f32_16x16x32_bf16 v[16:19], v[156:159], v[228:231], v[16:19]
	v_mfma_f32_16x16x32_bf16 v[12:15], v[164:167], v[228:231], v[12:15]
	v_mfma_f32_16x16x32_bf16 v[8:11], v[156:159], v[236:239], v[8:11]
	v_mfma_f32_16x16x32_bf16 v[4:7], v[164:167], v[236:239], v[4:7]
	s_setprio 0
	s_setprio 1
	v_mfma_f32_16x16x32_bf16 v[68:71], v[168:171], v[184:187], v[68:71]
	v_mfma_f32_16x16x32_bf16 v[76:79], v[176:179], v[184:187], v[76:79]
	v_mfma_f32_16x16x32_bf16 v[60:63], v[168:171], v[212:215], v[60:63]
	v_mfma_f32_16x16x32_bf16 v[64:67], v[176:179], v[212:215], v[64:67]
	v_mfma_f32_16x16x32_bf16 v[44:47], v[168:171], v[224:227], v[44:47]
	v_mfma_f32_16x16x32_bf16 v[48:51], v[176:179], v[224:227], v[48:51]
	v_mfma_f32_16x16x32_bf16 v[32:35], v[168:171], v[232:235], v[32:35]
	v_mfma_f32_16x16x32_bf16 v[40:43], v[176:179], v[232:235], v[40:43]
	s_setprio 0
	s_setprio 1
	v_mfma_f32_16x16x32_bf16 v[68:71], v[172:175], v[190:193], v[68:71]
	v_mfma_f32_16x16x32_bf16 v[76:79], v[180:183], v[190:193], v[76:79]
	v_mfma_f32_16x16x32_bf16 v[60:63], v[172:175], v[216:219], v[60:63]
	v_mfma_f32_16x16x32_bf16 v[64:67], v[180:183], v[216:219], v[64:67]
	v_mfma_f32_16x16x32_bf16 v[44:47], v[172:175], v[228:231], v[44:47]
	v_mfma_f32_16x16x32_bf16 v[48:51], v[180:183], v[228:231], v[48:51]
	v_mfma_f32_16x16x32_bf16 v[32:35], v[172:175], v[236:239], v[32:35]
	v_mfma_f32_16x16x32_bf16 v[40:43], v[180:183], v[236:239], v[40:43]
